# speedup vs baseline: 1.0123x; 1.0007x over previous
_Z7gemm128ILi2ELi128EEv8GemmArgs:
	s_cmp_ge_u32 s2, 0x100
	s_cbranch_scc1 .Lup_exit
	s_load_dwordx4 s[4:7], s[0:1], 0x0
	s_load_dwordx2 s[8:9], s[0:1], 0x20
	s_load_dwordx2 s[10:11], s[0:1], 0x48
	s_and_b32 s12, s2, 7
	s_lshr_b32 s13, s2, 3
	s_lshl_b32 s12, s12, 5
	s_add_u32 s12, s12, s13
	s_and_b32 s13, s12, 3
	s_lshr_b32 s12, s12, 2
	s_lshl_b32 s12, s12, 7
	s_lshl_b32 s13, s13, 8
	s_add_u32 s13, s13, 0x800
	s_mov_b32 s24, 0xc0135761
	s_mov_b32 s26, 0x3dd2d3e8
	s_mov_b32 s27, 0x3dd2d3e8
	s_mov_b32 s28, 0xc0135761
	s_mov_b32 s29, 0xc0135761
	s_mov_b32 s30, 1.0
	s_mov_b32 s31, 1.0
	v_lshrrev_b32_e32 v1, 6, v0
	v_and_b32_e32 v24, 7, v0
	v_bfe_u32 v25, v0, 4, 3
	v_xor_b32_e32 v24, v24, v25
	v_readfirstlane_b32 s14, v1
	v_lshrrev_b32_e32 v25, 3, v0
	v_mul_u32_u24_e32 v25, 0x600, v25
	v_lshl_add_u32 v2, v24, 4, v25
	s_mov_b32 s22, 0xc000
	v_add_u32_e32 v3, s22, v2
	v_add_u32_e32 v4, s22, v3
	v_add_u32_e32 v5, s22, v4
	v_add_u32_e32 v6, s22, v5
	v_add_u32_e32 v7, s22, v6
	v_add_u32_e32 v8, s22, v7
	v_add_u32_e32 v9, s22, v8
	v_and_b32_e32 v24, 15, v0
	v_bfe_u32 v25, v0, 4, 2
	v_lshrrev_b32_e32 v26, 1, v24
	v_xor_b32_e32 v26, v26, v25
	v_lshlrev_b32_e32 v26, 4, v26
	v_bfe_u32 v27, v0, 7, 1
	v_bfe_u32 v28, v0, 6, 1
	v_lshl_add_u32 v29, v27, 6, v24
	v_lshl_add_u32 v10, v29, 7, v26
	v_lshl_add_u32 v30, v28, 7, v24
	v_lshl_add_u32 v11, v30, 7, v26
	v_add_u32_e32 v11, 0x4000, v11
	v_add_u32_e32 v29, s12, v29
	v_lshlrev_b32_e32 v21, 6, v29
	v_mul_u32_u24_e32 v29, 0x1800, v29
	v_lshlrev_b32_e32 v30, 7, v28
	v_lshl_add_u32 v30, v25, 2, v30
	v_add_u32_e32 v30, s13, v30
	v_lshl_add_u32 v16, v30, 1, v29
	s_mov_b32 s22, 0x18000
	v_add_u32_e32 v17, s22, v16
	v_add_u32_e32 v18, s22, v17
	v_add_u32_e32 v19, s22, v18
	s_waitcnt lgkmcnt(0)
	s_mul_i32 s22, s12, 0x600
	s_add_u32 s16, s4, s22
	s_addc_u32 s17, s5, 0
	s_mul_i32 s22, s13, 0x600
	s_add_u32 s18, s6, s22
	s_addc_u32 s19, s7, 0
	s_lshl_b32 s20, s14, 10
	s_mov_b32 s21, 0
	s_add_u32 m0, s20, 0x0
	s_nop 0
	global_load_lds_dwordx4 v2, s[16:17]
	s_add_u32 m0, s20, 0x1000
	s_nop 0
	global_load_lds_dwordx4 v3, s[16:17]
	s_add_u32 m0, s20, 0x2000
	s_nop 0
	global_load_lds_dwordx4 v4, s[16:17]
	s_add_u32 m0, s20, 0x3000
	s_nop 0
	global_load_lds_dwordx4 v5, s[16:17]
	s_add_u32 m0, s20, 0x4000
	s_nop 0
	global_load_lds_dwordx4 v2, s[18:19]
	s_add_u32 m0, s20, 0x5000
	s_nop 0
	global_load_lds_dwordx4 v3, s[18:19]
	s_add_u32 m0, s20, 0x6000
	s_nop 0
	global_load_lds_dwordx4 v4, s[18:19]
	s_add_u32 m0, s20, 0x7000
	s_nop 0
	global_load_lds_dwordx4 v5, s[18:19]
	s_add_u32 m0, s20, 0x8000
	s_nop 0
	global_load_lds_dwordx4 v6, s[18:19]
	s_add_u32 m0, s20, 0x9000
	s_nop 0
	global_load_lds_dwordx4 v7, s[18:19]
	s_add_u32 m0, s20, 0xa000
	s_nop 0
	global_load_lds_dwordx4 v8, s[18:19]
	s_add_u32 m0, s20, 0xb000
	s_nop 0
	global_load_lds_dwordx4 v9, s[18:19]
	s_add_u32 s16, s16, 0x80
	s_addc_u32 s17, s17, 0
	s_add_u32 s18, s18, 0x80
	s_addc_u32 s19, s19, 0
	s_add_u32 s20, s20, 0xc000
	s_sub_u32 s22, s20, 0x24000
	s_cmp_ge_u32 s20, 0x24000
	s_cselect_b32 s20, s22, s20
	s_add_u32 m0, s20, 0x0
	s_nop 0
	global_load_lds_dwordx4 v2, s[16:17]
	s_add_u32 m0, s20, 0x1000
	s_nop 0
	global_load_lds_dwordx4 v3, s[16:17]
	s_add_u32 m0, s20, 0x2000
	s_nop 0
	global_load_lds_dwordx4 v4, s[16:17]
	s_add_u32 m0, s20, 0x3000
	s_nop 0
	global_load_lds_dwordx4 v5, s[16:17]
	s_add_u32 m0, s20, 0x4000
	s_nop 0
	global_load_lds_dwordx4 v2, s[18:19]
	s_add_u32 m0, s20, 0x5000
	s_nop 0
	global_load_lds_dwordx4 v3, s[18:19]
	s_add_u32 m0, s20, 0x6000
	s_nop 0
	global_load_lds_dwordx4 v4, s[18:19]
	s_add_u32 m0, s20, 0x7000
	s_nop 0
	global_load_lds_dwordx4 v5, s[18:19]
	s_add_u32 m0, s20, 0x8000
	s_nop 0
	global_load_lds_dwordx4 v6, s[18:19]
	s_add_u32 m0, s20, 0x9000
	s_nop 0
	global_load_lds_dwordx4 v7, s[18:19]
	s_add_u32 m0, s20, 0xa000
	s_nop 0
	global_load_lds_dwordx4 v8, s[18:19]
	s_add_u32 m0, s20, 0xb000
	s_nop 0
	global_load_lds_dwordx4 v9, s[18:19]
	s_add_u32 s16, s16, 0x80
	s_addc_u32 s17, s17, 0
	s_add_u32 s18, s18, 0x80
	s_addc_u32 s19, s19, 0
	s_add_u32 s20, s20, 0xc000
	s_sub_u32 s22, s20, 0x24000
	s_cmp_ge_u32 s20, 0x24000
	s_cselect_b32 s20, s22, s20
	s_add_u32 m0, s20, 0x0
	s_nop 0
	global_load_lds_dwordx4 v2, s[16:17]
	s_add_u32 m0, s20, 0x1000
	s_nop 0
	global_load_lds_dwordx4 v3, s[16:17]
	s_add_u32 m0, s20, 0x2000
	s_nop 0
	global_load_lds_dwordx4 v4, s[16:17]
	s_add_u32 m0, s20, 0x3000
	s_nop 0
	global_load_lds_dwordx4 v5, s[16:17]
	s_add_u32 m0, s20, 0x4000
	s_nop 0
	global_load_lds_dwordx4 v2, s[18:19]
	s_add_u32 m0, s20, 0x5000
	s_nop 0
	global_load_lds_dwordx4 v3, s[18:19]
	v_mov_b32_e32 v128, 0
	v_mov_b32_e32 v129, 0
	v_mov_b32_e32 v130, 0
	v_mov_b32_e32 v131, 0
	v_mov_b32_e32 v132, 0
	v_mov_b32_e32 v133, 0
	v_mov_b32_e32 v134, 0
	v_mov_b32_e32 v135, 0
	v_mov_b32_e32 v136, 0
	v_mov_b32_e32 v137, 0
	v_mov_b32_e32 v138, 0
	v_mov_b32_e32 v139, 0
	v_mov_b32_e32 v140, 0
	v_mov_b32_e32 v141, 0
	v_mov_b32_e32 v142, 0
	v_mov_b32_e32 v143, 0
	v_mov_b32_e32 v144, 0
	v_mov_b32_e32 v145, 0
	v_mov_b32_e32 v146, 0
	v_mov_b32_e32 v147, 0
	v_mov_b32_e32 v148, 0
	v_mov_b32_e32 v149, 0
	v_mov_b32_e32 v150, 0
	v_mov_b32_e32 v151, 0
	v_mov_b32_e32 v152, 0
	v_mov_b32_e32 v153, 0
	v_mov_b32_e32 v154, 0
	v_mov_b32_e32 v155, 0
	v_mov_b32_e32 v156, 0
	v_mov_b32_e32 v157, 0
	v_mov_b32_e32 v158, 0
	v_mov_b32_e32 v159, 0
	v_mov_b32_e32 v160, 0
	v_mov_b32_e32 v161, 0
	v_mov_b32_e32 v162, 0
	v_mov_b32_e32 v163, 0
	v_mov_b32_e32 v164, 0
	v_mov_b32_e32 v165, 0
	v_mov_b32_e32 v166, 0
	v_mov_b32_e32 v167, 0
	v_mov_b32_e32 v168, 0
	v_mov_b32_e32 v169, 0
	v_mov_b32_e32 v170, 0
	v_mov_b32_e32 v171, 0
	v_mov_b32_e32 v172, 0
	v_mov_b32_e32 v173, 0
	v_mov_b32_e32 v174, 0
	v_mov_b32_e32 v175, 0
	v_mov_b32_e32 v176, 0
	v_mov_b32_e32 v177, 0
	v_mov_b32_e32 v178, 0
	v_mov_b32_e32 v179, 0
	v_mov_b32_e32 v180, 0
	v_mov_b32_e32 v181, 0
	v_mov_b32_e32 v182, 0
	v_mov_b32_e32 v183, 0
	v_mov_b32_e32 v184, 0
	v_mov_b32_e32 v185, 0
	v_mov_b32_e32 v186, 0
	v_mov_b32_e32 v187, 0
	v_mov_b32_e32 v188, 0
	v_mov_b32_e32 v189, 0
	v_mov_b32_e32 v190, 0
	v_mov_b32_e32 v191, 0
	v_mov_b32_e32 v192, 0
	v_mov_b32_e32 v193, 0
	v_mov_b32_e32 v194, 0
	v_mov_b32_e32 v195, 0
	v_mov_b32_e32 v196, 0
	v_mov_b32_e32 v197, 0
	v_mov_b32_e32 v198, 0
	v_mov_b32_e32 v199, 0
	v_mov_b32_e32 v200, 0
	v_mov_b32_e32 v201, 0
	v_mov_b32_e32 v202, 0
	v_mov_b32_e32 v203, 0
	v_mov_b32_e32 v204, 0
	v_mov_b32_e32 v205, 0
	v_mov_b32_e32 v206, 0
	v_mov_b32_e32 v207, 0
	v_mov_b32_e32 v208, 0
	v_mov_b32_e32 v209, 0
	v_mov_b32_e32 v210, 0
	v_mov_b32_e32 v211, 0
	v_mov_b32_e32 v212, 0
	v_mov_b32_e32 v213, 0
	v_mov_b32_e32 v214, 0
	v_mov_b32_e32 v215, 0
	v_mov_b32_e32 v216, 0
	v_mov_b32_e32 v217, 0
	v_mov_b32_e32 v218, 0
	v_mov_b32_e32 v219, 0
	v_mov_b32_e32 v220, 0
	v_mov_b32_e32 v221, 0
	v_mov_b32_e32 v222, 0
	v_mov_b32_e32 v223, 0
	v_mov_b32_e32 v224, 0
	v_mov_b32_e32 v225, 0
	v_mov_b32_e32 v226, 0
	v_mov_b32_e32 v227, 0
	v_mov_b32_e32 v228, 0
	v_mov_b32_e32 v229, 0
	v_mov_b32_e32 v230, 0
	v_mov_b32_e32 v231, 0
	v_mov_b32_e32 v232, 0
	v_mov_b32_e32 v233, 0
	v_mov_b32_e32 v234, 0
	v_mov_b32_e32 v235, 0
	v_mov_b32_e32 v236, 0
	v_mov_b32_e32 v237, 0
	v_mov_b32_e32 v238, 0
	v_mov_b32_e32 v239, 0
	v_mov_b32_e32 v240, 0
	v_mov_b32_e32 v241, 0
	v_mov_b32_e32 v242, 0
	v_mov_b32_e32 v243, 0
	v_mov_b32_e32 v244, 0
	v_mov_b32_e32 v245, 0
	v_mov_b32_e32 v246, 0
	v_mov_b32_e32 v247, 0
	v_mov_b32_e32 v248, 0
	v_mov_b32_e32 v249, 0
	v_mov_b32_e32 v250, 0
	v_mov_b32_e32 v251, 0
	v_mov_b32_e32 v252, 0
	v_mov_b32_e32 v253, 0
	v_mov_b32_e32 v254, 0
	v_mov_b32_e32 v255, 0
	s_waitcnt vmcnt(18)
	s_barrier
	v_add_u32_e32 v12, s21, v10
	v_add_u32_e32 v14, s21, v11
	v_xor_b32_e32 v13, 64, v12
	v_xor_b32_e32 v15, 64, v14
	s_add_u32 s21, s21, 0xc000
	s_sub_u32 s23, s21, 0x24000
	s_cmp_ge_u32 s21, 0x24000
	s_cselect_b32 s21, s23, s21
	ds_read_b128 v[32:35], v12 offset:0
	ds_read_b128 v[36:39], v12 offset:2048
	ds_read_b128 v[40:43], v12 offset:4096
	ds_read_b128 v[44:47], v12 offset:6144
	ds_read_b128 v[48:51], v14 offset:0
	ds_read_b128 v[52:55], v14 offset:2048
	ds_read_b128 v[56:59], v14 offset:4096
	ds_read_b128 v[60:63], v14 offset:6144
	ds_read_b128 v[64:67], v14 offset:8192
	ds_read_b128 v[68:71], v14 offset:10240
	ds_read_b128 v[72:75], v14 offset:12288
	ds_read_b128 v[76:79], v14 offset:14336
	s_mov_b32 s15, 0
.Lup_loop:
	s_waitcnt lgkmcnt(0)
	v_mfma_f32_16x16x32_bf16 v[128:131], v[48:51], v[32:35], v[128:131]
	ds_read_b128 v[80:83], v13 offset:0
	v_mfma_f32_16x16x32_bf16 v[132:135], v[48:51], v[36:39], v[132:135]
	s_add_u32 m0, s20, 0x6000
	v_mfma_f32_16x16x32_bf16 v[136:139], v[48:51], v[40:43], v[136:139]
	ds_read_b128 v[84:87], v13 offset:2048
	v_mfma_f32_16x16x32_bf16 v[140:143], v[48:51], v[44:47], v[140:143]
	global_load_lds_dwordx4 v4, s[18:19]
	v_mfma_f32_16x16x32_bf16 v[144:147], v[52:55], v[32:35], v[144:147]
	ds_read_b128 v[88:91], v13 offset:4096
	v_mfma_f32_16x16x32_bf16 v[148:151], v[52:55], v[36:39], v[148:151]
	s_add_u32 m0, s20, 0x7000
	v_mfma_f32_16x16x32_bf16 v[152:155], v[52:55], v[40:43], v[152:155]
	ds_read_b128 v[92:95], v13 offset:6144
	v_mfma_f32_16x16x32_bf16 v[156:159], v[52:55], v[44:47], v[156:159]
	global_load_lds_dwordx4 v5, s[18:19]
	v_mfma_f32_16x16x32_bf16 v[160:163], v[56:59], v[32:35], v[160:163]
	ds_read_b128 v[96:99], v15 offset:0
	v_mfma_f32_16x16x32_bf16 v[164:167], v[56:59], v[36:39], v[164:167]
	s_add_u32 m0, s20, 0x8000
	v_mfma_f32_16x16x32_bf16 v[168:171], v[56:59], v[40:43], v[168:171]
	ds_read_b128 v[100:103], v15 offset:2048
	v_mfma_f32_16x16x32_bf16 v[172:175], v[56:59], v[44:47], v[172:175]
	global_load_lds_dwordx4 v6, s[18:19]
	v_mfma_f32_16x16x32_bf16 v[176:179], v[60:63], v[32:35], v[176:179]
	ds_read_b128 v[104:107], v15 offset:4096
	v_mfma_f32_16x16x32_bf16 v[180:183], v[60:63], v[36:39], v[180:183]
	s_add_u32 m0, s20, 0x9000
	v_mfma_f32_16x16x32_bf16 v[184:187], v[60:63], v[40:43], v[184:187]
	ds_read_b128 v[108:111], v15 offset:6144
	v_mfma_f32_16x16x32_bf16 v[188:191], v[60:63], v[44:47], v[188:191]
	global_load_lds_dwordx4 v7, s[18:19]
	v_mfma_f32_16x16x32_bf16 v[192:195], v[64:67], v[32:35], v[192:195]
	ds_read_b128 v[112:115], v15 offset:8192
	v_mfma_f32_16x16x32_bf16 v[196:199], v[64:67], v[36:39], v[196:199]
	s_add_u32 m0, s20, 0xa000
	v_mfma_f32_16x16x32_bf16 v[200:203], v[64:67], v[40:43], v[200:203]
	ds_read_b128 v[116:119], v15 offset:10240
	v_mfma_f32_16x16x32_bf16 v[204:207], v[64:67], v[44:47], v[204:207]
	global_load_lds_dwordx4 v8, s[18:19]
	v_mfma_f32_16x16x32_bf16 v[208:211], v[68:71], v[32:35], v[208:211]
	ds_read_b128 v[120:123], v15 offset:12288
	v_mfma_f32_16x16x32_bf16 v[212:215], v[68:71], v[36:39], v[212:215]
	s_add_u32 m0, s20, 0xb000
	v_mfma_f32_16x16x32_bf16 v[216:219], v[68:71], v[40:43], v[216:219]
	ds_read_b128 v[124:127], v15 offset:14336
	v_mfma_f32_16x16x32_bf16 v[220:223], v[68:71], v[44:47], v[220:223]
	global_load_lds_dwordx4 v9, s[18:19]
	v_mfma_f32_16x16x32_bf16 v[224:227], v[72:75], v[32:35], v[224:227]
	v_mfma_f32_16x16x32_bf16 v[228:231], v[72:75], v[36:39], v[228:231]
	v_mfma_f32_16x16x32_bf16 v[232:235], v[72:75], v[40:43], v[232:235]
	v_mfma_f32_16x16x32_bf16 v[236:239], v[72:75], v[44:47], v[236:239]
	v_mfma_f32_16x16x32_bf16 v[240:243], v[76:79], v[32:35], v[240:243]
	s_add_u32 s16, s16, 0x80
	s_addc_u32 s17, s17, 0
	s_add_u32 s18, s18, 0x80
	s_addc_u32 s19, s19, 0
	v_mfma_f32_16x16x32_bf16 v[244:247], v[76:79], v[36:39], v[244:247]
	s_add_u32 s20, s20, 0xc000
	s_sub_u32 s22, s20, 0x24000
	s_cmp_ge_u32 s20, 0x24000
	s_cselect_b32 s20, s22, s20
	v_mfma_f32_16x16x32_bf16 v[248:251], v[76:79], v[40:43], v[248:251]
	v_add_u32_e32 v12, s21, v10
	v_add_u32_e32 v14, s21, v11
	v_xor_b32_e32 v13, 64, v12
	v_xor_b32_e32 v15, 64, v14
	v_mfma_f32_16x16x32_bf16 v[252:255], v[76:79], v[44:47], v[252:255]
	s_add_u32 s21, s21, 0xc000
	s_sub_u32 s23, s21, 0x24000
	s_cmp_ge_u32 s21, 0x24000
	s_cselect_b32 s21, s23, s21
	s_waitcnt vmcnt(12) lgkmcnt(0)
	s_barrier
	v_mfma_f32_16x16x32_bf16 v[128:131], v[96:99], v[80:83], v[128:131]
	ds_read_b128 v[32:35], v12 offset:0
	v_mfma_f32_16x16x32_bf16 v[132:135], v[96:99], v[84:87], v[132:135]
	s_add_u32 m0, s20, 0x0
	v_mfma_f32_16x16x32_bf16 v[136:139], v[96:99], v[88:91], v[136:139]
	ds_read_b128 v[36:39], v12 offset:2048
	v_mfma_f32_16x16x32_bf16 v[140:143], v[96:99], v[92:95], v[140:143]
	global_load_lds_dwordx4 v2, s[16:17]
	v_mfma_f32_16x16x32_bf16 v[144:147], v[100:103], v[80:83], v[144:147]
	ds_read_b128 v[40:43], v12 offset:4096
	v_mfma_f32_16x16x32_bf16 v[148:151], v[100:103], v[84:87], v[148:151]
	s_add_u32 m0, s20, 0x1000
	v_mfma_f32_16x16x32_bf16 v[152:155], v[100:103], v[88:91], v[152:155]
	ds_read_b128 v[44:47], v12 offset:6144
	v_mfma_f32_16x16x32_bf16 v[156:159], v[100:103], v[92:95], v[156:159]
	global_load_lds_dwordx4 v3, s[16:17]
	v_mfma_f32_16x16x32_bf16 v[160:163], v[104:107], v[80:83], v[160:163]
	ds_read_b128 v[48:51], v14 offset:0
	v_mfma_f32_16x16x32_bf16 v[164:167], v[104:107], v[84:87], v[164:167]
	s_add_u32 m0, s20, 0x2000
	v_mfma_f32_16x16x32_bf16 v[168:171], v[104:107], v[88:91], v[168:171]
	ds_read_b128 v[52:55], v14 offset:2048
	v_mfma_f32_16x16x32_bf16 v[172:175], v[104:107], v[92:95], v[172:175]
	global_load_lds_dwordx4 v4, s[16:17]
	v_mfma_f32_16x16x32_bf16 v[176:179], v[108:111], v[80:83], v[176:179]
	ds_read_b128 v[56:59], v14 offset:4096
	v_mfma_f32_16x16x32_bf16 v[180:183], v[108:111], v[84:87], v[180:183]
	s_add_u32 m0, s20, 0x3000
	v_mfma_f32_16x16x32_bf16 v[184:187], v[108:111], v[88:91], v[184:187]
	ds_read_b128 v[60:63], v14 offset:6144
	v_mfma_f32_16x16x32_bf16 v[188:191], v[108:111], v[92:95], v[188:191]
	global_load_lds_dwordx4 v5, s[16:17]
	v_mfma_f32_16x16x32_bf16 v[192:195], v[112:115], v[80:83], v[192:195]
	ds_read_b128 v[64:67], v14 offset:8192
	v_mfma_f32_16x16x32_bf16 v[196:199], v[112:115], v[84:87], v[196:199]
	s_add_u32 m0, s20, 0x4000
	v_mfma_f32_16x16x32_bf16 v[200:203], v[112:115], v[88:91], v[200:203]
	ds_read_b128 v[68:71], v14 offset:10240
	v_mfma_f32_16x16x32_bf16 v[204:207], v[112:115], v[92:95], v[204:207]
	global_load_lds_dwordx4 v2, s[18:19]
	v_mfma_f32_16x16x32_bf16 v[208:211], v[116:119], v[80:83], v[208:211]
	ds_read_b128 v[72:75], v14 offset:12288
	v_mfma_f32_16x16x32_bf16 v[212:215], v[116:119], v[84:87], v[212:215]
	s_add_u32 m0, s20, 0x5000
	v_mfma_f32_16x16x32_bf16 v[216:219], v[116:119], v[88:91], v[216:219]
	ds_read_b128 v[76:79], v14 offset:14336
	v_mfma_f32_16x16x32_bf16 v[220:223], v[116:119], v[92:95], v[220:223]
	global_load_lds_dwordx4 v3, s[18:19]
	v_mfma_f32_16x16x32_bf16 v[224:227], v[120:123], v[80:83], v[224:227]
	v_mfma_f32_16x16x32_bf16 v[228:231], v[120:123], v[84:87], v[228:231]
	v_mfma_f32_16x16x32_bf16 v[232:235], v[120:123], v[88:91], v[232:235]
	v_mfma_f32_16x16x32_bf16 v[236:239], v[120:123], v[92:95], v[236:239]
	v_mfma_f32_16x16x32_bf16 v[240:243], v[124:127], v[80:83], v[240:243]
	v_mfma_f32_16x16x32_bf16 v[244:247], v[124:127], v[84:87], v[244:247]
	v_mfma_f32_16x16x32_bf16 v[248:251], v[124:127], v[88:91], v[248:251]
	v_mfma_f32_16x16x32_bf16 v[252:255], v[124:127], v[92:95], v[252:255]
	s_add_u32 s15, s15, 1
	s_cmp_lt_u32 s15, 9
	s_cbranch_scc1 .Lup_loop
	s_waitcnt lgkmcnt(0)
	v_mfma_f32_16x16x32_bf16 v[128:131], v[48:51], v[32:35], v[128:131]
	ds_read_b128 v[80:83], v13 offset:0
	v_mfma_f32_16x16x32_bf16 v[132:135], v[48:51], v[36:39], v[132:135]
	s_add_u32 m0, s20, 0x6000
	v_mfma_f32_16x16x32_bf16 v[136:139], v[48:51], v[40:43], v[136:139]
	ds_read_b128 v[84:87], v13 offset:2048
	v_mfma_f32_16x16x32_bf16 v[140:143], v[48:51], v[44:47], v[140:143]
	global_load_lds_dwordx4 v4, s[18:19]
	v_mfma_f32_16x16x32_bf16 v[144:147], v[52:55], v[32:35], v[144:147]
	ds_read_b128 v[88:91], v13 offset:4096
	v_mfma_f32_16x16x32_bf16 v[148:151], v[52:55], v[36:39], v[148:151]
	s_add_u32 m0, s20, 0x7000
	v_mfma_f32_16x16x32_bf16 v[152:155], v[52:55], v[40:43], v[152:155]
	ds_read_b128 v[92:95], v13 offset:6144
	v_mfma_f32_16x16x32_bf16 v[156:159], v[52:55], v[44:47], v[156:159]
	global_load_lds_dwordx4 v5, s[18:19]
	v_mfma_f32_16x16x32_bf16 v[160:163], v[56:59], v[32:35], v[160:163]
	ds_read_b128 v[96:99], v15 offset:0
	v_mfma_f32_16x16x32_bf16 v[164:167], v[56:59], v[36:39], v[164:167]
	s_add_u32 m0, s20, 0x8000
	v_mfma_f32_16x16x32_bf16 v[168:171], v[56:59], v[40:43], v[168:171]
	ds_read_b128 v[100:103], v15 offset:2048
	v_mfma_f32_16x16x32_bf16 v[172:175], v[56:59], v[44:47], v[172:175]
	global_load_lds_dwordx4 v6, s[18:19]
	v_mfma_f32_16x16x32_bf16 v[176:179], v[60:63], v[32:35], v[176:179]
	ds_read_b128 v[104:107], v15 offset:4096
	v_mfma_f32_16x16x32_bf16 v[180:183], v[60:63], v[36:39], v[180:183]
	s_add_u32 m0, s20, 0x9000
	v_mfma_f32_16x16x32_bf16 v[184:187], v[60:63], v[40:43], v[184:187]
	ds_read_b128 v[108:111], v15 offset:6144
	v_mfma_f32_16x16x32_bf16 v[188:191], v[60:63], v[44:47], v[188:191]
	global_load_lds_dwordx4 v7, s[18:19]
	v_mfma_f32_16x16x32_bf16 v[192:195], v[64:67], v[32:35], v[192:195]
	ds_read_b128 v[112:115], v15 offset:8192
	v_mfma_f32_16x16x32_bf16 v[196:199], v[64:67], v[36:39], v[196:199]
	s_add_u32 m0, s20, 0xa000
	v_mfma_f32_16x16x32_bf16 v[200:203], v[64:67], v[40:43], v[200:203]
	ds_read_b128 v[116:119], v15 offset:10240
	v_mfma_f32_16x16x32_bf16 v[204:207], v[64:67], v[44:47], v[204:207]
	global_load_lds_dwordx4 v8, s[18:19]
	v_mfma_f32_16x16x32_bf16 v[208:211], v[68:71], v[32:35], v[208:211]
	ds_read_b128 v[120:123], v15 offset:12288
	v_mfma_f32_16x16x32_bf16 v[212:215], v[68:71], v[36:39], v[212:215]
	s_add_u32 m0, s20, 0xb000
	v_mfma_f32_16x16x32_bf16 v[216:219], v[68:71], v[40:43], v[216:219]
	ds_read_b128 v[124:127], v15 offset:14336
	v_mfma_f32_16x16x32_bf16 v[220:223], v[68:71], v[44:47], v[220:223]
	global_load_lds_dwordx4 v9, s[18:19]
	v_mfma_f32_16x16x32_bf16 v[224:227], v[72:75], v[32:35], v[224:227]
	v_mfma_f32_16x16x32_bf16 v[228:231], v[72:75], v[36:39], v[228:231]
	v_mfma_f32_16x16x32_bf16 v[232:235], v[72:75], v[40:43], v[232:235]
	v_mfma_f32_16x16x32_bf16 v[236:239], v[72:75], v[44:47], v[236:239]
	v_mfma_f32_16x16x32_bf16 v[240:243], v[76:79], v[32:35], v[240:243]
	s_add_u32 s16, s16, 0x80
	s_addc_u32 s17, s17, 0
	s_add_u32 s18, s18, 0x80
	s_addc_u32 s19, s19, 0
	v_mfma_f32_16x16x32_bf16 v[244:247], v[76:79], v[36:39], v[244:247]
	s_add_u32 s20, s20, 0xc000
	s_sub_u32 s22, s20, 0x24000
	s_cmp_ge_u32 s20, 0x24000
	s_cselect_b32 s20, s22, s20
	v_mfma_f32_16x16x32_bf16 v[248:251], v[76:79], v[40:43], v[248:251]
	v_add_u32_e32 v12, s21, v10
	v_add_u32_e32 v14, s21, v11
	v_xor_b32_e32 v13, 64, v12
	v_xor_b32_e32 v15, 64, v14
	v_mfma_f32_16x16x32_bf16 v[252:255], v[76:79], v[44:47], v[252:255]
	s_add_u32 s21, s21, 0xc000
	s_sub_u32 s23, s21, 0x24000
	s_cmp_ge_u32 s21, 0x24000
	s_cselect_b32 s21, s23, s21
	s_waitcnt vmcnt(12) lgkmcnt(0)
	s_barrier
	v_mfma_f32_16x16x32_bf16 v[128:131], v[96:99], v[80:83], v[128:131]
	ds_read_b128 v[32:35], v12 offset:0
	v_mfma_f32_16x16x32_bf16 v[132:135], v[96:99], v[84:87], v[132:135]
	ds_read_b128 v[36:39], v12 offset:2048
	v_mfma_f32_16x16x32_bf16 v[136:139], v[96:99], v[88:91], v[136:139]
	ds_read_b128 v[40:43], v12 offset:4096
	v_mfma_f32_16x16x32_bf16 v[140:143], v[96:99], v[92:95], v[140:143]
	ds_read_b128 v[44:47], v12 offset:6144
	v_mfma_f32_16x16x32_bf16 v[144:147], v[100:103], v[80:83], v[144:147]
	ds_read_b128 v[48:51], v14 offset:0
	v_mfma_f32_16x16x32_bf16 v[148:151], v[100:103], v[84:87], v[148:151]
	ds_read_b128 v[52:55], v14 offset:2048
	v_mfma_f32_16x16x32_bf16 v[152:155], v[100:103], v[88:91], v[152:155]
	ds_read_b128 v[56:59], v14 offset:4096
	v_mfma_f32_16x16x32_bf16 v[156:159], v[100:103], v[92:95], v[156:159]
	ds_read_b128 v[60:63], v14 offset:6144
	v_mfma_f32_16x16x32_bf16 v[160:163], v[104:107], v[80:83], v[160:163]
	ds_read_b128 v[64:67], v14 offset:8192
	v_mfma_f32_16x16x32_bf16 v[164:167], v[104:107], v[84:87], v[164:167]
	ds_read_b128 v[68:71], v14 offset:10240
	v_mfma_f32_16x16x32_bf16 v[168:171], v[104:107], v[88:91], v[168:171]
	ds_read_b128 v[72:75], v14 offset:12288
	v_mfma_f32_16x16x32_bf16 v[172:175], v[104:107], v[92:95], v[172:175]
	ds_read_b128 v[76:79], v14 offset:14336
	v_mfma_f32_16x16x32_bf16 v[176:179], v[108:111], v[80:83], v[176:179]
	v_mfma_f32_16x16x32_bf16 v[180:183], v[108:111], v[84:87], v[180:183]
	v_mfma_f32_16x16x32_bf16 v[184:187], v[108:111], v[88:91], v[184:187]
	v_mfma_f32_16x16x32_bf16 v[188:191], v[108:111], v[92:95], v[188:191]
	v_mfma_f32_16x16x32_bf16 v[192:195], v[112:115], v[80:83], v[192:195]
	v_mfma_f32_16x16x32_bf16 v[196:199], v[112:115], v[84:87], v[196:199]
	v_mfma_f32_16x16x32_bf16 v[200:203], v[112:115], v[88:91], v[200:203]
	v_mfma_f32_16x16x32_bf16 v[204:207], v[112:115], v[92:95], v[204:207]
	v_mfma_f32_16x16x32_bf16 v[208:211], v[116:119], v[80:83], v[208:211]
	v_mfma_f32_16x16x32_bf16 v[212:215], v[116:119], v[84:87], v[212:215]
	v_mfma_f32_16x16x32_bf16 v[216:219], v[116:119], v[88:91], v[216:219]
	v_mfma_f32_16x16x32_bf16 v[220:223], v[116:119], v[92:95], v[220:223]
	v_mfma_f32_16x16x32_bf16 v[224:227], v[120:123], v[80:83], v[224:227]
	v_mfma_f32_16x16x32_bf16 v[228:231], v[120:123], v[84:87], v[228:231]
	v_mfma_f32_16x16x32_bf16 v[232:235], v[120:123], v[88:91], v[232:235]
	v_mfma_f32_16x16x32_bf16 v[236:239], v[120:123], v[92:95], v[236:239]
	v_mfma_f32_16x16x32_bf16 v[240:243], v[124:127], v[80:83], v[240:243]
	v_mfma_f32_16x16x32_bf16 v[244:247], v[124:127], v[84:87], v[244:247]
	v_mfma_f32_16x16x32_bf16 v[248:251], v[124:127], v[88:91], v[248:251]
	v_mfma_f32_16x16x32_bf16 v[252:255], v[124:127], v[92:95], v[252:255]
	s_waitcnt lgkmcnt(0)
	v_mfma_f32_16x16x32_bf16 v[128:131], v[48:51], v[32:35], v[128:131]
	ds_read_b128 v[80:83], v13 offset:0
	v_mfma_f32_16x16x32_bf16 v[132:135], v[48:51], v[36:39], v[132:135]
	ds_read_b128 v[84:87], v13 offset:2048
	v_mfma_f32_16x16x32_bf16 v[136:139], v[48:51], v[40:43], v[136:139]
	ds_read_b128 v[88:91], v13 offset:4096
	v_mfma_f32_16x16x32_bf16 v[140:143], v[48:51], v[44:47], v[140:143]
	ds_read_b128 v[92:95], v13 offset:6144
	v_mfma_f32_16x16x32_bf16 v[144:147], v[52:55], v[32:35], v[144:147]
	ds_read_b128 v[96:99], v15 offset:0
	v_mfma_f32_16x16x32_bf16 v[148:151], v[52:55], v[36:39], v[148:151]
	ds_read_b128 v[100:103], v15 offset:2048
	v_mfma_f32_16x16x32_bf16 v[152:155], v[52:55], v[40:43], v[152:155]
	ds_read_b128 v[104:107], v15 offset:4096
	v_mfma_f32_16x16x32_bf16 v[156:159], v[52:55], v[44:47], v[156:159]
	ds_read_b128 v[108:111], v15 offset:6144
	v_mfma_f32_16x16x32_bf16 v[160:163], v[56:59], v[32:35], v[160:163]
	ds_read_b128 v[112:115], v15 offset:8192
	v_mfma_f32_16x16x32_bf16 v[164:167], v[56:59], v[36:39], v[164:167]
	ds_read_b128 v[116:119], v15 offset:10240
	v_mfma_f32_16x16x32_bf16 v[168:171], v[56:59], v[40:43], v[168:171]
	ds_read_b128 v[120:123], v15 offset:12288
	v_mfma_f32_16x16x32_bf16 v[172:175], v[56:59], v[44:47], v[172:175]
	ds_read_b128 v[124:127], v15 offset:14336
	v_mfma_f32_16x16x32_bf16 v[176:179], v[60:63], v[32:35], v[176:179]
	v_mfma_f32_16x16x32_bf16 v[180:183], v[60:63], v[36:39], v[180:183]
	v_mfma_f32_16x16x32_bf16 v[184:187], v[60:63], v[40:43], v[184:187]
	v_mfma_f32_16x16x32_bf16 v[188:191], v[60:63], v[44:47], v[188:191]
	v_mfma_f32_16x16x32_bf16 v[192:195], v[64:67], v[32:35], v[192:195]
	v_mfma_f32_16x16x32_bf16 v[196:199], v[64:67], v[36:39], v[196:199]
	v_mfma_f32_16x16x32_bf16 v[200:203], v[64:67], v[40:43], v[200:203]
	v_mfma_f32_16x16x32_bf16 v[204:207], v[64:67], v[44:47], v[204:207]
	v_mfma_f32_16x16x32_bf16 v[208:211], v[68:71], v[32:35], v[208:211]
	v_mfma_f32_16x16x32_bf16 v[212:215], v[68:71], v[36:39], v[212:215]
	v_mfma_f32_16x16x32_bf16 v[216:219], v[68:71], v[40:43], v[216:219]
	v_mfma_f32_16x16x32_bf16 v[220:223], v[68:71], v[44:47], v[220:223]
	v_mfma_f32_16x16x32_bf16 v[224:227], v[72:75], v[32:35], v[224:227]
	v_mfma_f32_16x16x32_bf16 v[228:231], v[72:75], v[36:39], v[228:231]
	v_mfma_f32_16x16x32_bf16 v[232:235], v[72:75], v[40:43], v[232:235]
	v_mfma_f32_16x16x32_bf16 v[236:239], v[72:75], v[44:47], v[236:239]
	v_mfma_f32_16x16x32_bf16 v[240:243], v[76:79], v[32:35], v[240:243]
	v_add_u32_e32 v12, s21, v10
	v_add_u32_e32 v14, s21, v11
	v_xor_b32_e32 v13, 64, v12
	v_xor_b32_e32 v15, 64, v14
	v_mfma_f32_16x16x32_bf16 v[244:247], v[76:79], v[36:39], v[244:247]
	s_add_u32 s21, s21, 0xc000
	s_sub_u32 s23, s21, 0x24000
	s_cmp_ge_u32 s21, 0x24000
	s_cselect_b32 s21, s23, s21
	v_mfma_f32_16x16x32_bf16 v[248:251], v[76:79], v[40:43], v[248:251]
	v_mfma_f32_16x16x32_bf16 v[252:255], v[76:79], v[44:47], v[252:255]
	s_waitcnt vmcnt(0) lgkmcnt(0)
	s_barrier
	v_mfma_f32_16x16x32_bf16 v[128:131], v[96:99], v[80:83], v[128:131]
	ds_read_b128 v[32:35], v12 offset:0
	v_mfma_f32_16x16x32_bf16 v[132:135], v[96:99], v[84:87], v[132:135]
	ds_read_b128 v[36:39], v12 offset:2048
	v_mfma_f32_16x16x32_bf16 v[136:139], v[96:99], v[88:91], v[136:139]
	ds_read_b128 v[40:43], v12 offset:4096
	v_mfma_f32_16x16x32_bf16 v[140:143], v[96:99], v[92:95], v[140:143]
	ds_read_b128 v[44:47], v12 offset:6144
	v_mfma_f32_16x16x32_bf16 v[144:147], v[100:103], v[80:83], v[144:147]
	ds_read_b128 v[48:51], v14 offset:0
	v_mfma_f32_16x16x32_bf16 v[148:151], v[100:103], v[84:87], v[148:151]
	ds_read_b128 v[52:55], v14 offset:2048
	v_mfma_f32_16x16x32_bf16 v[152:155], v[100:103], v[88:91], v[152:155]
	ds_read_b128 v[56:59], v14 offset:4096
	v_mfma_f32_16x16x32_bf16 v[156:159], v[100:103], v[92:95], v[156:159]
	ds_read_b128 v[60:63], v14 offset:6144
	v_mfma_f32_16x16x32_bf16 v[160:163], v[104:107], v[80:83], v[160:163]
	ds_read_b128 v[64:67], v14 offset:8192
	v_mfma_f32_16x16x32_bf16 v[164:167], v[104:107], v[84:87], v[164:167]
	ds_read_b128 v[68:71], v14 offset:10240
	v_mfma_f32_16x16x32_bf16 v[168:171], v[104:107], v[88:91], v[168:171]
	ds_read_b128 v[72:75], v14 offset:12288
	v_mfma_f32_16x16x32_bf16 v[172:175], v[104:107], v[92:95], v[172:175]
	ds_read_b128 v[76:79], v14 offset:14336
	v_mfma_f32_16x16x32_bf16 v[176:179], v[108:111], v[80:83], v[176:179]
	v_mfma_f32_16x16x32_bf16 v[180:183], v[108:111], v[84:87], v[180:183]
	v_mfma_f32_16x16x32_bf16 v[184:187], v[108:111], v[88:91], v[184:187]
	v_mfma_f32_16x16x32_bf16 v[188:191], v[108:111], v[92:95], v[188:191]
	v_mfma_f32_16x16x32_bf16 v[192:195], v[112:115], v[80:83], v[192:195]
	v_mfma_f32_16x16x32_bf16 v[196:199], v[112:115], v[84:87], v[196:199]
	v_mfma_f32_16x16x32_bf16 v[200:203], v[112:115], v[88:91], v[200:203]
	v_mfma_f32_16x16x32_bf16 v[204:207], v[112:115], v[92:95], v[204:207]
	v_mfma_f32_16x16x32_bf16 v[208:211], v[116:119], v[80:83], v[208:211]
	v_mfma_f32_16x16x32_bf16 v[212:215], v[116:119], v[84:87], v[212:215]
	v_mfma_f32_16x16x32_bf16 v[216:219], v[116:119], v[88:91], v[216:219]
	v_mfma_f32_16x16x32_bf16 v[220:223], v[116:119], v[92:95], v[220:223]
	v_mfma_f32_16x16x32_bf16 v[224:227], v[120:123], v[80:83], v[224:227]
	v_mfma_f32_16x16x32_bf16 v[228:231], v[120:123], v[84:87], v[228:231]
	v_mfma_f32_16x16x32_bf16 v[232:235], v[120:123], v[88:91], v[232:235]
	v_mfma_f32_16x16x32_bf16 v[236:239], v[120:123], v[92:95], v[236:239]
	v_mfma_f32_16x16x32_bf16 v[240:243], v[124:127], v[80:83], v[240:243]
	v_mfma_f32_16x16x32_bf16 v[244:247], v[124:127], v[84:87], v[244:247]
	v_mfma_f32_16x16x32_bf16 v[248:251], v[124:127], v[88:91], v[248:251]
	v_mfma_f32_16x16x32_bf16 v[252:255], v[124:127], v[92:95], v[252:255]
	s_waitcnt lgkmcnt(0)
	v_mfma_f32_16x16x32_bf16 v[128:131], v[48:51], v[32:35], v[128:131]
	ds_read_b128 v[80:83], v13 offset:0
	v_mfma_f32_16x16x32_bf16 v[132:135], v[48:51], v[36:39], v[132:135]
	ds_read_b128 v[84:87], v13 offset:2048
	v_mfma_f32_16x16x32_bf16 v[136:139], v[48:51], v[40:43], v[136:139]
	ds_read_b128 v[88:91], v13 offset:4096
	v_mfma_f32_16x16x32_bf16 v[140:143], v[48:51], v[44:47], v[140:143]
	ds_read_b128 v[92:95], v13 offset:6144
	v_mfma_f32_16x16x32_bf16 v[144:147], v[52:55], v[32:35], v[144:147]
	ds_read_b128 v[96:99], v15 offset:0
	v_mfma_f32_16x16x32_bf16 v[148:151], v[52:55], v[36:39], v[148:151]
	ds_read_b128 v[100:103], v15 offset:2048
	v_mfma_f32_16x16x32_bf16 v[152:155], v[52:55], v[40:43], v[152:155]
	ds_read_b128 v[104:107], v15 offset:4096
	v_mfma_f32_16x16x32_bf16 v[156:159], v[52:55], v[44:47], v[156:159]
	ds_read_b128 v[108:111], v15 offset:6144
	v_mfma_f32_16x16x32_bf16 v[160:163], v[56:59], v[32:35], v[160:163]
	ds_read_b128 v[112:115], v15 offset:8192
	v_mfma_f32_16x16x32_bf16 v[164:167], v[56:59], v[36:39], v[164:167]
	ds_read_b128 v[116:119], v15 offset:10240
	v_mfma_f32_16x16x32_bf16 v[168:171], v[56:59], v[40:43], v[168:171]
	ds_read_b128 v[120:123], v15 offset:12288
	v_mfma_f32_16x16x32_bf16 v[172:175], v[56:59], v[44:47], v[172:175]
	ds_read_b128 v[124:127], v15 offset:14336
	v_mfma_f32_16x16x32_bf16 v[176:179], v[60:63], v[32:35], v[176:179]
	v_mfma_f32_16x16x32_bf16 v[180:183], v[60:63], v[36:39], v[180:183]
	v_mfma_f32_16x16x32_bf16 v[184:187], v[60:63], v[40:43], v[184:187]
	v_mfma_f32_16x16x32_bf16 v[188:191], v[60:63], v[44:47], v[188:191]
	v_mfma_f32_16x16x32_bf16 v[192:195], v[64:67], v[32:35], v[192:195]
	v_mfma_f32_16x16x32_bf16 v[196:199], v[64:67], v[36:39], v[196:199]
	v_mfma_f32_16x16x32_bf16 v[200:203], v[64:67], v[40:43], v[200:203]
	v_mfma_f32_16x16x32_bf16 v[204:207], v[64:67], v[44:47], v[204:207]
	v_mfma_f32_16x16x32_bf16 v[208:211], v[68:71], v[32:35], v[208:211]
	v_mfma_f32_16x16x32_bf16 v[212:215], v[68:71], v[36:39], v[212:215]
	v_mfma_f32_16x16x32_bf16 v[216:219], v[68:71], v[40:43], v[216:219]
	v_mfma_f32_16x16x32_bf16 v[220:223], v[68:71], v[44:47], v[220:223]
	v_mfma_f32_16x16x32_bf16 v[224:227], v[72:75], v[32:35], v[224:227]
	v_mfma_f32_16x16x32_bf16 v[228:231], v[72:75], v[36:39], v[228:231]
	v_mfma_f32_16x16x32_bf16 v[232:235], v[72:75], v[40:43], v[232:235]
	v_mfma_f32_16x16x32_bf16 v[236:239], v[72:75], v[44:47], v[236:239]
	v_mfma_f32_16x16x32_bf16 v[240:243], v[76:79], v[32:35], v[240:243]
	v_mfma_f32_16x16x32_bf16 v[244:247], v[76:79], v[36:39], v[244:247]
	v_mfma_f32_16x16x32_bf16 v[248:251], v[76:79], v[40:43], v[248:251]
	v_mfma_f32_16x16x32_bf16 v[252:255], v[76:79], v[44:47], v[252:255]
	s_waitcnt lgkmcnt(0)
	v_mfma_f32_16x16x32_bf16 v[128:131], v[96:99], v[80:83], v[128:131]
	v_mfma_f32_16x16x32_bf16 v[132:135], v[96:99], v[84:87], v[132:135]
	global_load_dwordx4 v[32:35], v21, s[8:9] offset:0
	v_mfma_f32_16x16x32_bf16 v[136:139], v[96:99], v[88:91], v[136:139]
	v_mfma_f32_16x16x32_bf16 v[140:143], v[96:99], v[92:95], v[140:143]
	global_load_dwordx4 v[36:39], v21, s[8:9] offset:16
	v_mfma_f32_16x16x32_bf16 v[144:147], v[100:103], v[80:83], v[144:147]
	v_mfma_f32_16x16x32_bf16 v[148:151], v[100:103], v[84:87], v[148:151]
	global_load_dwordx4 v[40:43], v21, s[8:9] offset:32
	v_mfma_f32_16x16x32_bf16 v[152:155], v[100:103], v[88:91], v[152:155]
	v_mfma_f32_16x16x32_bf16 v[156:159], v[100:103], v[92:95], v[156:159]
	global_load_dwordx4 v[44:47], v21, s[8:9] offset:48
	v_mfma_f32_16x16x32_bf16 v[160:163], v[104:107], v[80:83], v[160:163]
	v_mfma_f32_16x16x32_bf16 v[164:167], v[104:107], v[84:87], v[164:167]
	global_load_dwordx4 v[48:51], v21, s[8:9] offset:1024
	v_mfma_f32_16x16x32_bf16 v[168:171], v[104:107], v[88:91], v[168:171]
	v_mfma_f32_16x16x32_bf16 v[172:175], v[104:107], v[92:95], v[172:175]
	global_load_dwordx4 v[52:55], v21, s[8:9] offset:1040
	v_mfma_f32_16x16x32_bf16 v[176:179], v[108:111], v[80:83], v[176:179]
	v_mfma_f32_16x16x32_bf16 v[180:183], v[108:111], v[84:87], v[180:183]
	global_load_dwordx4 v[56:59], v21, s[8:9] offset:1056
	v_mfma_f32_16x16x32_bf16 v[184:187], v[108:111], v[88:91], v[184:187]
	v_mfma_f32_16x16x32_bf16 v[188:191], v[108:111], v[92:95], v[188:191]
	global_load_dwordx4 v[60:63], v21, s[8:9] offset:1072
	v_mfma_f32_16x16x32_bf16 v[192:195], v[112:115], v[80:83], v[192:195]
	v_mfma_f32_16x16x32_bf16 v[196:199], v[112:115], v[84:87], v[196:199]
	global_load_dwordx4 v[64:67], v21, s[8:9] offset:2048
	v_mfma_f32_16x16x32_bf16 v[200:203], v[112:115], v[88:91], v[200:203]
	v_mfma_f32_16x16x32_bf16 v[204:207], v[112:115], v[92:95], v[204:207]
	global_load_dwordx4 v[68:71], v21, s[8:9] offset:2064
	v_mfma_f32_16x16x32_bf16 v[208:211], v[116:119], v[80:83], v[208:211]
	v_mfma_f32_16x16x32_bf16 v[212:215], v[116:119], v[84:87], v[212:215]
	global_load_dwordx4 v[72:75], v21, s[8:9] offset:2080
	v_mfma_f32_16x16x32_bf16 v[216:219], v[116:119], v[88:91], v[216:219]
	v_mfma_f32_16x16x32_bf16 v[220:223], v[116:119], v[92:95], v[220:223]
	global_load_dwordx4 v[76:79], v21, s[8:9] offset:2096
	v_mfma_f32_16x16x32_bf16 v[224:227], v[120:123], v[80:83], v[224:227]
	v_mfma_f32_16x16x32_bf16 v[228:231], v[120:123], v[84:87], v[228:231]
	v_mfma_f32_16x16x32_bf16 v[232:235], v[120:123], v[88:91], v[232:235]
	v_mfma_f32_16x16x32_bf16 v[236:239], v[120:123], v[92:95], v[236:239]
	v_mfma_f32_16x16x32_bf16 v[240:243], v[124:127], v[80:83], v[240:243]
	v_mfma_f32_16x16x32_bf16 v[244:247], v[124:127], v[84:87], v[244:247]
	v_mfma_f32_16x16x32_bf16 v[248:251], v[124:127], v[88:91], v[248:251]
	v_mfma_f32_16x16x32_bf16 v[252:255], v[124:127], v[92:95], v[252:255]
	global_load_dwordx4 v[80:83], v21, s[8:9] offset:3072
	global_load_dwordx4 v[84:87], v21, s[8:9] offset:3088
	global_load_dwordx4 v[88:91], v21, s[8:9] offset:3104
	global_load_dwordx4 v[92:95], v21, s[8:9] offset:3120
	v_mov_b32_e32 v31, 0x358637bd
	s_waitcnt vmcnt(0)
	v_add_f32_e32 v32, v32, v33
	v_add_f32_e32 v34, v34, v35
	v_add_f32_e32 v36, v36, v37
	v_add_f32_e32 v38, v38, v39
	v_add_f32_e32 v40, v40, v41
	v_add_f32_e32 v42, v42, v43
	v_add_f32_e32 v44, v44, v45
	v_add_f32_e32 v46, v46, v47
	v_add_f32_e32 v32, v32, v34
	v_add_f32_e32 v36, v36, v38
	v_add_f32_e32 v40, v40, v42
	v_add_f32_e32 v44, v44, v46
	v_add_f32_e32 v32, v32, v36
	v_add_f32_e32 v40, v40, v44
	s_nop 0
	v_add_f32_e32 v32, v32, v40
	v_add_f32_e32 v48, v48, v49
	v_add_f32_e32 v50, v50, v51
	v_add_f32_e32 v52, v52, v53
	v_add_f32_e32 v54, v54, v55
	v_add_f32_e32 v56, v56, v57
	v_add_f32_e32 v58, v58, v59
	v_add_f32_e32 v60, v60, v61
	v_add_f32_e32 v62, v62, v63
	v_add_f32_e32 v48, v48, v50
	v_add_f32_e32 v52, v52, v54
	v_add_f32_e32 v56, v56, v58
	v_add_f32_e32 v60, v60, v62
	v_add_f32_e32 v48, v48, v52
	v_add_f32_e32 v56, v56, v60
	s_nop 0
	v_add_f32_e32 v48, v48, v56
	v_add_f32_e32 v64, v64, v65
	v_add_f32_e32 v66, v66, v67
	v_add_f32_e32 v68, v68, v69
	v_add_f32_e32 v70, v70, v71
	v_add_f32_e32 v72, v72, v73
	v_add_f32_e32 v74, v74, v75
	v_add_f32_e32 v76, v76, v77
	v_add_f32_e32 v78, v78, v79
	v_add_f32_e32 v64, v64, v66
	v_add_f32_e32 v68, v68, v70
	v_add_f32_e32 v72, v72, v74
	v_add_f32_e32 v76, v76, v78
	v_add_f32_e32 v64, v64, v68
	v_add_f32_e32 v72, v72, v76
	s_nop 0
	v_add_f32_e32 v64, v64, v72
	v_add_f32_e32 v80, v80, v81
	v_add_f32_e32 v82, v82, v83
	v_add_f32_e32 v84, v84, v85
	v_add_f32_e32 v86, v86, v87
	v_add_f32_e32 v88, v88, v89
	v_add_f32_e32 v90, v90, v91
	v_add_f32_e32 v92, v92, v93
	v_add_f32_e32 v94, v94, v95
	v_add_f32_e32 v80, v80, v82
	v_add_f32_e32 v84, v84, v86
	v_add_f32_e32 v88, v88, v90
	v_add_f32_e32 v92, v92, v94
	v_add_f32_e32 v80, v80, v84
	v_add_f32_e32 v88, v88, v92
	s_nop 0
	v_add_f32_e32 v80, v80, v88
	v_fmamk_f32 v20, v32, 0x3aaaaaab, v31
	v_fmamk_f32 v22, v48, 0x3aaaaaab, v31
	v_fmamk_f32 v24, v64, 0x3aaaaaab, v31
	v_fmamk_f32 v26, v80, 0x3aaaaaab, v31
	v_rsq_f32_e32 v20, v20
	v_rsq_f32_e32 v22, v22
	v_rsq_f32_e32 v24, v24
	v_rsq_f32_e32 v26, v26
	s_nop 0
	v_pk_mul_f32 v[128:129], v[128:129], v[20:21] op_sel_hi:[1,0]
	v_pk_mul_f32 v[130:131], v[130:131], v[20:21] op_sel_hi:[1,0]
	v_pk_mul_f32 v[144:145], v[144:145], v[20:21] op_sel_hi:[1,0]
	v_pk_mul_f32 v[146:147], v[146:147], v[20:21] op_sel_hi:[1,0]
	v_pk_mul_f32 v[32:33], v[128:129], s[26:27]
	v_pk_mul_f32 v[34:35], v[130:131], s[26:27]
	v_pk_mul_f32 v[36:37], v[144:145], s[26:27]
	v_pk_mul_f32 v[38:39], v[146:147], s[26:27]
	v_pk_fma_f32 v[32:33], v[128:129], v[32:33], s[28:29] neg_lo:[1,0,0] neg_hi:[1,0,0]
	v_pk_fma_f32 v[34:35], v[130:131], v[34:35], s[28:29] neg_lo:[1,0,0] neg_hi:[1,0,0]
	v_pk_fma_f32 v[36:37], v[144:145], v[36:37], s[28:29] neg_lo:[1,0,0] neg_hi:[1,0,0]
	v_pk_fma_f32 v[38:39], v[146:147], v[38:39], s[28:29] neg_lo:[1,0,0] neg_hi:[1,0,0]
	v_pk_mul_f32 v[32:33], v[128:129], v[32:33]
	v_pk_mul_f32 v[34:35], v[130:131], v[34:35]
	v_pk_mul_f32 v[36:37], v[144:145], v[36:37]
	v_pk_mul_f32 v[38:39], v[146:147], v[38:39]
	v_exp_f32_e32 v32, v32
	v_exp_f32_e32 v33, v33
	v_exp_f32_e32 v34, v34
	v_exp_f32_e32 v35, v35
	v_exp_f32_e32 v36, v36
	v_exp_f32_e32 v37, v37
	v_exp_f32_e32 v38, v38
	v_exp_f32_e32 v39, v39
	v_pk_add_f32 v[32:33], v[32:33], s[30:31]
	v_pk_add_f32 v[34:35], v[34:35], s[30:31]
	v_pk_add_f32 v[36:37], v[36:37], s[30:31]
	v_pk_add_f32 v[38:39], v[38:39], s[30:31]
	v_rcp_f32_e32 v32, v32
	v_rcp_f32_e32 v33, v33
	v_rcp_f32_e32 v34, v34
	v_rcp_f32_e32 v35, v35
	v_rcp_f32_e32 v36, v36
	v_rcp_f32_e32 v37, v37
	v_rcp_f32_e32 v38, v38
	v_rcp_f32_e32 v39, v39
	s_nop 0
	v_pk_mul_f32 v[128:129], v[128:129], v[32:33]
	v_pk_mul_f32 v[130:131], v[130:131], v[34:35]
	v_pk_mul_f32 v[144:145], v[144:145], v[36:37]
	v_pk_mul_f32 v[146:147], v[146:147], v[38:39]
	v_cvt_pk_bf16_f32 v64, v128, v129
	v_cvt_pk_bf16_f32 v65, v130, v131
	v_cvt_pk_bf16_f32 v66, v144, v145
	v_cvt_pk_bf16_f32 v67, v146, v147
	global_store_dwordx2 v16, v[64:65], s[10:11]
	global_store_dwordx2 v16, v[66:67], s[10:11] offset:32
	v_pk_mul_f32 v[160:161], v[160:161], v[20:21] op_sel_hi:[1,0]
	v_pk_mul_f32 v[162:163], v[162:163], v[20:21] op_sel_hi:[1,0]
	v_pk_mul_f32 v[176:177], v[176:177], v[20:21] op_sel_hi:[1,0]
	v_pk_mul_f32 v[178:179], v[178:179], v[20:21] op_sel_hi:[1,0]
	v_pk_mul_f32 v[48:49], v[160:161], s[26:27]
	v_pk_mul_f32 v[50:51], v[162:163], s[26:27]
	v_pk_mul_f32 v[52:53], v[176:177], s[26:27]
	v_pk_mul_f32 v[54:55], v[178:179], s[26:27]
	v_pk_fma_f32 v[48:49], v[160:161], v[48:49], s[28:29] neg_lo:[1,0,0] neg_hi:[1,0,0]
	v_pk_fma_f32 v[50:51], v[162:163], v[50:51], s[28:29] neg_lo:[1,0,0] neg_hi:[1,0,0]
	v_pk_fma_f32 v[52:53], v[176:177], v[52:53], s[28:29] neg_lo:[1,0,0] neg_hi:[1,0,0]
	v_pk_fma_f32 v[54:55], v[178:179], v[54:55], s[28:29] neg_lo:[1,0,0] neg_hi:[1,0,0]
	v_pk_mul_f32 v[48:49], v[160:161], v[48:49]
	v_pk_mul_f32 v[50:51], v[162:163], v[50:51]
	v_pk_mul_f32 v[52:53], v[176:177], v[52:53]
	v_pk_mul_f32 v[54:55], v[178:179], v[54:55]
	v_exp_f32_e32 v48, v48
	v_exp_f32_e32 v49, v49
	v_exp_f32_e32 v50, v50
	v_exp_f32_e32 v51, v51
	v_exp_f32_e32 v52, v52
	v_exp_f32_e32 v53, v53
	v_exp_f32_e32 v54, v54
	v_exp_f32_e32 v55, v55
	v_pk_add_f32 v[48:49], v[48:49], s[30:31]
	v_pk_add_f32 v[50:51], v[50:51], s[30:31]
	v_pk_add_f32 v[52:53], v[52:53], s[30:31]
	v_pk_add_f32 v[54:55], v[54:55], s[30:31]
	v_rcp_f32_e32 v48, v48
	v_rcp_f32_e32 v49, v49
	v_rcp_f32_e32 v50, v50
	v_rcp_f32_e32 v51, v51
	v_rcp_f32_e32 v52, v52
	v_rcp_f32_e32 v53, v53
	v_rcp_f32_e32 v54, v54
	v_rcp_f32_e32 v55, v55
	s_nop 0
	v_pk_mul_f32 v[160:161], v[160:161], v[48:49]
	v_pk_mul_f32 v[162:163], v[162:163], v[50:51]
	v_pk_mul_f32 v[176:177], v[176:177], v[52:53]
	v_pk_mul_f32 v[178:179], v[178:179], v[54:55]
	v_cvt_pk_bf16_f32 v68, v160, v161
	v_cvt_pk_bf16_f32 v69, v162, v163
	v_cvt_pk_bf16_f32 v70, v176, v177
	v_cvt_pk_bf16_f32 v71, v178, v179
	global_store_dwordx2 v16, v[68:69], s[10:11] offset:64
	global_store_dwordx2 v16, v[70:71], s[10:11] offset:96
	v_pk_mul_f32 v[192:193], v[192:193], v[20:21] op_sel_hi:[1,0]
	v_pk_mul_f32 v[194:195], v[194:195], v[20:21] op_sel_hi:[1,0]
	v_pk_mul_f32 v[208:209], v[208:209], v[20:21] op_sel_hi:[1,0]
	v_pk_mul_f32 v[210:211], v[210:211], v[20:21] op_sel_hi:[1,0]
	v_pk_mul_f32 v[32:33], v[192:193], s[26:27]
	v_pk_mul_f32 v[34:35], v[194:195], s[26:27]
	v_pk_mul_f32 v[36:37], v[208:209], s[26:27]
	v_pk_mul_f32 v[38:39], v[210:211], s[26:27]
	v_pk_fma_f32 v[32:33], v[192:193], v[32:33], s[28:29] neg_lo:[1,0,0] neg_hi:[1,0,0]
	v_pk_fma_f32 v[34:35], v[194:195], v[34:35], s[28:29] neg_lo:[1,0,0] neg_hi:[1,0,0]
	v_pk_fma_f32 v[36:37], v[208:209], v[36:37], s[28:29] neg_lo:[1,0,0] neg_hi:[1,0,0]
	v_pk_fma_f32 v[38:39], v[210:211], v[38:39], s[28:29] neg_lo:[1,0,0] neg_hi:[1,0,0]
	v_pk_mul_f32 v[32:33], v[192:193], v[32:33]
	v_pk_mul_f32 v[34:35], v[194:195], v[34:35]
	v_pk_mul_f32 v[36:37], v[208:209], v[36:37]
	v_pk_mul_f32 v[38:39], v[210:211], v[38:39]
	v_exp_f32_e32 v32, v32
	v_exp_f32_e32 v33, v33
	v_exp_f32_e32 v34, v34
	v_exp_f32_e32 v35, v35
	v_exp_f32_e32 v36, v36
	v_exp_f32_e32 v37, v37
	v_exp_f32_e32 v38, v38
	v_exp_f32_e32 v39, v39
	v_pk_add_f32 v[32:33], v[32:33], s[30:31]
	v_pk_add_f32 v[34:35], v[34:35], s[30:31]
	v_pk_add_f32 v[36:37], v[36:37], s[30:31]
	v_pk_add_f32 v[38:39], v[38:39], s[30:31]
	v_rcp_f32_e32 v32, v32
	v_rcp_f32_e32 v33, v33
	v_rcp_f32_e32 v34, v34
	v_rcp_f32_e32 v35, v35
	v_rcp_f32_e32 v36, v36
	v_rcp_f32_e32 v37, v37
	v_rcp_f32_e32 v38, v38
	v_rcp_f32_e32 v39, v39
	s_nop 0
	v_pk_mul_f32 v[192:193], v[192:193], v[32:33]
	v_pk_mul_f32 v[194:195], v[194:195], v[34:35]
	v_pk_mul_f32 v[208:209], v[208:209], v[36:37]
	v_pk_mul_f32 v[210:211], v[210:211], v[38:39]
	v_cvt_pk_bf16_f32 v64, v192, v193
	v_cvt_pk_bf16_f32 v65, v194, v195
	v_cvt_pk_bf16_f32 v66, v208, v209
	v_cvt_pk_bf16_f32 v67, v210, v211
	global_store_dwordx2 v16, v[64:65], s[10:11] offset:128
	global_store_dwordx2 v16, v[66:67], s[10:11] offset:160
	v_pk_mul_f32 v[224:225], v[224:225], v[20:21] op_sel_hi:[1,0]
	v_pk_mul_f32 v[226:227], v[226:227], v[20:21] op_sel_hi:[1,0]
	v_pk_mul_f32 v[240:241], v[240:241], v[20:21] op_sel_hi:[1,0]
	v_pk_mul_f32 v[242:243], v[242:243], v[20:21] op_sel_hi:[1,0]
	v_pk_mul_f32 v[48:49], v[224:225], s[26:27]
	v_pk_mul_f32 v[50:51], v[226:227], s[26:27]
	v_pk_mul_f32 v[52:53], v[240:241], s[26:27]
	v_pk_mul_f32 v[54:55], v[242:243], s[26:27]
	v_pk_fma_f32 v[48:49], v[224:225], v[48:49], s[28:29] neg_lo:[1,0,0] neg_hi:[1,0,0]
	v_pk_fma_f32 v[50:51], v[226:227], v[50:51], s[28:29] neg_lo:[1,0,0] neg_hi:[1,0,0]
	v_pk_fma_f32 v[52:53], v[240:241], v[52:53], s[28:29] neg_lo:[1,0,0] neg_hi:[1,0,0]
	v_pk_fma_f32 v[54:55], v[242:243], v[54:55], s[28:29] neg_lo:[1,0,0] neg_hi:[1,0,0]
	v_pk_mul_f32 v[48:49], v[224:225], v[48:49]
	v_pk_mul_f32 v[50:51], v[226:227], v[50:51]
	v_pk_mul_f32 v[52:53], v[240:241], v[52:53]
	v_pk_mul_f32 v[54:55], v[242:243], v[54:55]
	v_exp_f32_e32 v48, v48
	v_exp_f32_e32 v49, v49
	v_exp_f32_e32 v50, v50
	v_exp_f32_e32 v51, v51
	v_exp_f32_e32 v52, v52
	v_exp_f32_e32 v53, v53
	v_exp_f32_e32 v54, v54
	v_exp_f32_e32 v55, v55
	v_pk_add_f32 v[48:49], v[48:49], s[30:31]
	v_pk_add_f32 v[50:51], v[50:51], s[30:31]
	v_pk_add_f32 v[52:53], v[52:53], s[30:31]
	v_pk_add_f32 v[54:55], v[54:55], s[30:31]
	v_rcp_f32_e32 v48, v48
	v_rcp_f32_e32 v49, v49
	v_rcp_f32_e32 v50, v50
	v_rcp_f32_e32 v51, v51
	v_rcp_f32_e32 v52, v52
	v_rcp_f32_e32 v53, v53
	v_rcp_f32_e32 v54, v54
	v_rcp_f32_e32 v55, v55
	s_nop 0
	v_pk_mul_f32 v[224:225], v[224:225], v[48:49]
	v_pk_mul_f32 v[226:227], v[226:227], v[50:51]
	v_pk_mul_f32 v[240:241], v[240:241], v[52:53]
	v_pk_mul_f32 v[242:243], v[242:243], v[54:55]
	v_cvt_pk_bf16_f32 v68, v224, v225
	v_cvt_pk_bf16_f32 v69, v226, v227
	v_cvt_pk_bf16_f32 v70, v240, v241
	v_cvt_pk_bf16_f32 v71, v242, v243
	global_store_dwordx2 v16, v[68:69], s[10:11] offset:192
	global_store_dwordx2 v16, v[70:71], s[10:11] offset:224
	v_pk_mul_f32 v[132:133], v[132:133], v[22:23] op_sel_hi:[1,0]
	v_pk_mul_f32 v[134:135], v[134:135], v[22:23] op_sel_hi:[1,0]
	v_pk_mul_f32 v[148:149], v[148:149], v[22:23] op_sel_hi:[1,0]
	v_pk_mul_f32 v[150:151], v[150:151], v[22:23] op_sel_hi:[1,0]
	v_pk_mul_f32 v[32:33], v[132:133], s[26:27]
	v_pk_mul_f32 v[34:35], v[134:135], s[26:27]
	v_pk_mul_f32 v[36:37], v[148:149], s[26:27]
	v_pk_mul_f32 v[38:39], v[150:151], s[26:27]
	v_pk_fma_f32 v[32:33], v[132:133], v[32:33], s[28:29] neg_lo:[1,0,0] neg_hi:[1,0,0]
	v_pk_fma_f32 v[34:35], v[134:135], v[34:35], s[28:29] neg_lo:[1,0,0] neg_hi:[1,0,0]
	v_pk_fma_f32 v[36:37], v[148:149], v[36:37], s[28:29] neg_lo:[1,0,0] neg_hi:[1,0,0]
	v_pk_fma_f32 v[38:39], v[150:151], v[38:39], s[28:29] neg_lo:[1,0,0] neg_hi:[1,0,0]
	v_pk_mul_f32 v[32:33], v[132:133], v[32:33]
	v_pk_mul_f32 v[34:35], v[134:135], v[34:35]
	v_pk_mul_f32 v[36:37], v[148:149], v[36:37]
	v_pk_mul_f32 v[38:39], v[150:151], v[38:39]
	v_exp_f32_e32 v32, v32
	v_exp_f32_e32 v33, v33
	v_exp_f32_e32 v34, v34
	v_exp_f32_e32 v35, v35
	v_exp_f32_e32 v36, v36
	v_exp_f32_e32 v37, v37
	v_exp_f32_e32 v38, v38
	v_exp_f32_e32 v39, v39
	v_pk_add_f32 v[32:33], v[32:33], s[30:31]
	v_pk_add_f32 v[34:35], v[34:35], s[30:31]
	v_pk_add_f32 v[36:37], v[36:37], s[30:31]
	v_pk_add_f32 v[38:39], v[38:39], s[30:31]
	v_rcp_f32_e32 v32, v32
	v_rcp_f32_e32 v33, v33
	v_rcp_f32_e32 v34, v34
	v_rcp_f32_e32 v35, v35
	v_rcp_f32_e32 v36, v36
	v_rcp_f32_e32 v37, v37
	v_rcp_f32_e32 v38, v38
	v_rcp_f32_e32 v39, v39
	s_nop 0
	v_pk_mul_f32 v[132:133], v[132:133], v[32:33]
	v_pk_mul_f32 v[134:135], v[134:135], v[34:35]
	v_pk_mul_f32 v[148:149], v[148:149], v[36:37]
	v_pk_mul_f32 v[150:151], v[150:151], v[38:39]
	v_cvt_pk_bf16_f32 v64, v132, v133
	v_cvt_pk_bf16_f32 v65, v134, v135
	v_cvt_pk_bf16_f32 v66, v148, v149
	v_cvt_pk_bf16_f32 v67, v150, v151
	global_store_dwordx2 v17, v[64:65], s[10:11]
	global_store_dwordx2 v17, v[66:67], s[10:11] offset:32
	v_pk_mul_f32 v[164:165], v[164:165], v[22:23] op_sel_hi:[1,0]
	v_pk_mul_f32 v[166:167], v[166:167], v[22:23] op_sel_hi:[1,0]
	v_pk_mul_f32 v[180:181], v[180:181], v[22:23] op_sel_hi:[1,0]
	v_pk_mul_f32 v[182:183], v[182:183], v[22:23] op_sel_hi:[1,0]
	v_pk_mul_f32 v[48:49], v[164:165], s[26:27]
	v_pk_mul_f32 v[50:51], v[166:167], s[26:27]
	v_pk_mul_f32 v[52:53], v[180:181], s[26:27]
	v_pk_mul_f32 v[54:55], v[182:183], s[26:27]
	v_pk_fma_f32 v[48:49], v[164:165], v[48:49], s[28:29] neg_lo:[1,0,0] neg_hi:[1,0,0]
	v_pk_fma_f32 v[50:51], v[166:167], v[50:51], s[28:29] neg_lo:[1,0,0] neg_hi:[1,0,0]
	v_pk_fma_f32 v[52:53], v[180:181], v[52:53], s[28:29] neg_lo:[1,0,0] neg_hi:[1,0,0]
	v_pk_fma_f32 v[54:55], v[182:183], v[54:55], s[28:29] neg_lo:[1,0,0] neg_hi:[1,0,0]
	v_pk_mul_f32 v[48:49], v[164:165], v[48:49]
	v_pk_mul_f32 v[50:51], v[166:167], v[50:51]
	v_pk_mul_f32 v[52:53], v[180:181], v[52:53]
	v_pk_mul_f32 v[54:55], v[182:183], v[54:55]
	v_exp_f32_e32 v48, v48
	v_exp_f32_e32 v49, v49
	v_exp_f32_e32 v50, v50
	v_exp_f32_e32 v51, v51
	v_exp_f32_e32 v52, v52
	v_exp_f32_e32 v53, v53
	v_exp_f32_e32 v54, v54
	v_exp_f32_e32 v55, v55
	v_pk_add_f32 v[48:49], v[48:49], s[30:31]
	v_pk_add_f32 v[50:51], v[50:51], s[30:31]
	v_pk_add_f32 v[52:53], v[52:53], s[30:31]
	v_pk_add_f32 v[54:55], v[54:55], s[30:31]
	v_rcp_f32_e32 v48, v48
	v_rcp_f32_e32 v49, v49
	v_rcp_f32_e32 v50, v50
	v_rcp_f32_e32 v51, v51
	v_rcp_f32_e32 v52, v52
	v_rcp_f32_e32 v53, v53
	v_rcp_f32_e32 v54, v54
	v_rcp_f32_e32 v55, v55
	s_nop 0
	v_pk_mul_f32 v[164:165], v[164:165], v[48:49]
	v_pk_mul_f32 v[166:167], v[166:167], v[50:51]
	v_pk_mul_f32 v[180:181], v[180:181], v[52:53]
	v_pk_mul_f32 v[182:183], v[182:183], v[54:55]
	v_cvt_pk_bf16_f32 v68, v164, v165
	v_cvt_pk_bf16_f32 v69, v166, v167
	v_cvt_pk_bf16_f32 v70, v180, v181
	v_cvt_pk_bf16_f32 v71, v182, v183
	global_store_dwordx2 v17, v[68:69], s[10:11] offset:64
	global_store_dwordx2 v17, v[70:71], s[10:11] offset:96
	v_pk_mul_f32 v[196:197], v[196:197], v[22:23] op_sel_hi:[1,0]
	v_pk_mul_f32 v[198:199], v[198:199], v[22:23] op_sel_hi:[1,0]
	v_pk_mul_f32 v[212:213], v[212:213], v[22:23] op_sel_hi:[1,0]
	v_pk_mul_f32 v[214:215], v[214:215], v[22:23] op_sel_hi:[1,0]
	v_pk_mul_f32 v[32:33], v[196:197], s[26:27]
	v_pk_mul_f32 v[34:35], v[198:199], s[26:27]
	v_pk_mul_f32 v[36:37], v[212:213], s[26:27]
	v_pk_mul_f32 v[38:39], v[214:215], s[26:27]
	v_pk_fma_f32 v[32:33], v[196:197], v[32:33], s[28:29] neg_lo:[1,0,0] neg_hi:[1,0,0]
	v_pk_fma_f32 v[34:35], v[198:199], v[34:35], s[28:29] neg_lo:[1,0,0] neg_hi:[1,0,0]
	v_pk_fma_f32 v[36:37], v[212:213], v[36:37], s[28:29] neg_lo:[1,0,0] neg_hi:[1,0,0]
	v_pk_fma_f32 v[38:39], v[214:215], v[38:39], s[28:29] neg_lo:[1,0,0] neg_hi:[1,0,0]
	v_pk_mul_f32 v[32:33], v[196:197], v[32:33]
	v_pk_mul_f32 v[34:35], v[198:199], v[34:35]
	v_pk_mul_f32 v[36:37], v[212:213], v[36:37]
	v_pk_mul_f32 v[38:39], v[214:215], v[38:39]
	v_exp_f32_e32 v32, v32
	v_exp_f32_e32 v33, v33
	v_exp_f32_e32 v34, v34
	v_exp_f32_e32 v35, v35
	v_exp_f32_e32 v36, v36
	v_exp_f32_e32 v37, v37
	v_exp_f32_e32 v38, v38
	v_exp_f32_e32 v39, v39
	v_pk_add_f32 v[32:33], v[32:33], s[30:31]
	v_pk_add_f32 v[34:35], v[34:35], s[30:31]
	v_pk_add_f32 v[36:37], v[36:37], s[30:31]
	v_pk_add_f32 v[38:39], v[38:39], s[30:31]
	v_rcp_f32_e32 v32, v32
	v_rcp_f32_e32 v33, v33
	v_rcp_f32_e32 v34, v34
	v_rcp_f32_e32 v35, v35
	v_rcp_f32_e32 v36, v36
	v_rcp_f32_e32 v37, v37
	v_rcp_f32_e32 v38, v38
	v_rcp_f32_e32 v39, v39
	s_nop 0
	v_pk_mul_f32 v[196:197], v[196:197], v[32:33]
	v_pk_mul_f32 v[198:199], v[198:199], v[34:35]
	v_pk_mul_f32 v[212:213], v[212:213], v[36:37]
	v_pk_mul_f32 v[214:215], v[214:215], v[38:39]
	v_cvt_pk_bf16_f32 v64, v196, v197
	v_cvt_pk_bf16_f32 v65, v198, v199
	v_cvt_pk_bf16_f32 v66, v212, v213
	v_cvt_pk_bf16_f32 v67, v214, v215
	global_store_dwordx2 v17, v[64:65], s[10:11] offset:128
	global_store_dwordx2 v17, v[66:67], s[10:11] offset:160
	v_pk_mul_f32 v[228:229], v[228:229], v[22:23] op_sel_hi:[1,0]
	v_pk_mul_f32 v[230:231], v[230:231], v[22:23] op_sel_hi:[1,0]
	v_pk_mul_f32 v[244:245], v[244:245], v[22:23] op_sel_hi:[1,0]
	v_pk_mul_f32 v[246:247], v[246:247], v[22:23] op_sel_hi:[1,0]
	v_pk_mul_f32 v[48:49], v[228:229], s[26:27]
	v_pk_mul_f32 v[50:51], v[230:231], s[26:27]
	v_pk_mul_f32 v[52:53], v[244:245], s[26:27]
	v_pk_mul_f32 v[54:55], v[246:247], s[26:27]
	v_pk_fma_f32 v[48:49], v[228:229], v[48:49], s[28:29] neg_lo:[1,0,0] neg_hi:[1,0,0]
	v_pk_fma_f32 v[50:51], v[230:231], v[50:51], s[28:29] neg_lo:[1,0,0] neg_hi:[1,0,0]
	v_pk_fma_f32 v[52:53], v[244:245], v[52:53], s[28:29] neg_lo:[1,0,0] neg_hi:[1,0,0]
	v_pk_fma_f32 v[54:55], v[246:247], v[54:55], s[28:29] neg_lo:[1,0,0] neg_hi:[1,0,0]
	v_pk_mul_f32 v[48:49], v[228:229], v[48:49]
	v_pk_mul_f32 v[50:51], v[230:231], v[50:51]
	v_pk_mul_f32 v[52:53], v[244:245], v[52:53]
	v_pk_mul_f32 v[54:55], v[246:247], v[54:55]
	v_exp_f32_e32 v48, v48
	v_exp_f32_e32 v49, v49
	v_exp_f32_e32 v50, v50
	v_exp_f32_e32 v51, v51
	v_exp_f32_e32 v52, v52
	v_exp_f32_e32 v53, v53
	v_exp_f32_e32 v54, v54
	v_exp_f32_e32 v55, v55
	v_pk_add_f32 v[48:49], v[48:49], s[30:31]
	v_pk_add_f32 v[50:51], v[50:51], s[30:31]
	v_pk_add_f32 v[52:53], v[52:53], s[30:31]
	v_pk_add_f32 v[54:55], v[54:55], s[30:31]
	v_rcp_f32_e32 v48, v48
	v_rcp_f32_e32 v49, v49
	v_rcp_f32_e32 v50, v50
	v_rcp_f32_e32 v51, v51
	v_rcp_f32_e32 v52, v52
	v_rcp_f32_e32 v53, v53
	v_rcp_f32_e32 v54, v54
	v_rcp_f32_e32 v55, v55
	s_nop 0
	v_pk_mul_f32 v[228:229], v[228:229], v[48:49]
	v_pk_mul_f32 v[230:231], v[230:231], v[50:51]
	v_pk_mul_f32 v[244:245], v[244:245], v[52:53]
	v_pk_mul_f32 v[246:247], v[246:247], v[54:55]
	v_cvt_pk_bf16_f32 v68, v228, v229
	v_cvt_pk_bf16_f32 v69, v230, v231
	v_cvt_pk_bf16_f32 v70, v244, v245
	v_cvt_pk_bf16_f32 v71, v246, v247
	global_store_dwordx2 v17, v[68:69], s[10:11] offset:192
	global_store_dwordx2 v17, v[70:71], s[10:11] offset:224
	v_pk_mul_f32 v[136:137], v[136:137], v[24:25] op_sel_hi:[1,0]
	v_pk_mul_f32 v[138:139], v[138:139], v[24:25] op_sel_hi:[1,0]
	v_pk_mul_f32 v[152:153], v[152:153], v[24:25] op_sel_hi:[1,0]
	v_pk_mul_f32 v[154:155], v[154:155], v[24:25] op_sel_hi:[1,0]
	v_pk_mul_f32 v[32:33], v[136:137], s[26:27]
	v_pk_mul_f32 v[34:35], v[138:139], s[26:27]
	v_pk_mul_f32 v[36:37], v[152:153], s[26:27]
	v_pk_mul_f32 v[38:39], v[154:155], s[26:27]
	v_pk_fma_f32 v[32:33], v[136:137], v[32:33], s[28:29] neg_lo:[1,0,0] neg_hi:[1,0,0]
	v_pk_fma_f32 v[34:35], v[138:139], v[34:35], s[28:29] neg_lo:[1,0,0] neg_hi:[1,0,0]
	v_pk_fma_f32 v[36:37], v[152:153], v[36:37], s[28:29] neg_lo:[1,0,0] neg_hi:[1,0,0]
	v_pk_fma_f32 v[38:39], v[154:155], v[38:39], s[28:29] neg_lo:[1,0,0] neg_hi:[1,0,0]
	v_pk_mul_f32 v[32:33], v[136:137], v[32:33]
	v_pk_mul_f32 v[34:35], v[138:139], v[34:35]
	v_pk_mul_f32 v[36:37], v[152:153], v[36:37]
	v_pk_mul_f32 v[38:39], v[154:155], v[38:39]
	v_exp_f32_e32 v32, v32
	v_exp_f32_e32 v33, v33
	v_exp_f32_e32 v34, v34
	v_exp_f32_e32 v35, v35
	v_exp_f32_e32 v36, v36
	v_exp_f32_e32 v37, v37
	v_exp_f32_e32 v38, v38
	v_exp_f32_e32 v39, v39
	v_pk_add_f32 v[32:33], v[32:33], s[30:31]
	v_pk_add_f32 v[34:35], v[34:35], s[30:31]
	v_pk_add_f32 v[36:37], v[36:37], s[30:31]
	v_pk_add_f32 v[38:39], v[38:39], s[30:31]
	v_rcp_f32_e32 v32, v32
	v_rcp_f32_e32 v33, v33
	v_rcp_f32_e32 v34, v34
	v_rcp_f32_e32 v35, v35
	v_rcp_f32_e32 v36, v36
	v_rcp_f32_e32 v37, v37
	v_rcp_f32_e32 v38, v38
	v_rcp_f32_e32 v39, v39
	s_nop 0
	v_pk_mul_f32 v[136:137], v[136:137], v[32:33]
	v_pk_mul_f32 v[138:139], v[138:139], v[34:35]
	v_pk_mul_f32 v[152:153], v[152:153], v[36:37]
	v_pk_mul_f32 v[154:155], v[154:155], v[38:39]
	v_cvt_pk_bf16_f32 v64, v136, v137
	v_cvt_pk_bf16_f32 v65, v138, v139
	v_cvt_pk_bf16_f32 v66, v152, v153
	v_cvt_pk_bf16_f32 v67, v154, v155
	global_store_dwordx2 v18, v[64:65], s[10:11]
	global_store_dwordx2 v18, v[66:67], s[10:11] offset:32
	v_pk_mul_f32 v[168:169], v[168:169], v[24:25] op_sel_hi:[1,0]
	v_pk_mul_f32 v[170:171], v[170:171], v[24:25] op_sel_hi:[1,0]
	v_pk_mul_f32 v[184:185], v[184:185], v[24:25] op_sel_hi:[1,0]
	v_pk_mul_f32 v[186:187], v[186:187], v[24:25] op_sel_hi:[1,0]
	v_pk_mul_f32 v[48:49], v[168:169], s[26:27]
	v_pk_mul_f32 v[50:51], v[170:171], s[26:27]
	v_pk_mul_f32 v[52:53], v[184:185], s[26:27]
	v_pk_mul_f32 v[54:55], v[186:187], s[26:27]
	v_pk_fma_f32 v[48:49], v[168:169], v[48:49], s[28:29] neg_lo:[1,0,0] neg_hi:[1,0,0]
	v_pk_fma_f32 v[50:51], v[170:171], v[50:51], s[28:29] neg_lo:[1,0,0] neg_hi:[1,0,0]
	v_pk_fma_f32 v[52:53], v[184:185], v[52:53], s[28:29] neg_lo:[1,0,0] neg_hi:[1,0,0]
	v_pk_fma_f32 v[54:55], v[186:187], v[54:55], s[28:29] neg_lo:[1,0,0] neg_hi:[1,0,0]
	v_pk_mul_f32 v[48:49], v[168:169], v[48:49]
	v_pk_mul_f32 v[50:51], v[170:171], v[50:51]
	v_pk_mul_f32 v[52:53], v[184:185], v[52:53]
	v_pk_mul_f32 v[54:55], v[186:187], v[54:55]
	v_exp_f32_e32 v48, v48
	v_exp_f32_e32 v49, v49
	v_exp_f32_e32 v50, v50
	v_exp_f32_e32 v51, v51
	v_exp_f32_e32 v52, v52
	v_exp_f32_e32 v53, v53
	v_exp_f32_e32 v54, v54
	v_exp_f32_e32 v55, v55
	v_pk_add_f32 v[48:49], v[48:49], s[30:31]
	v_pk_add_f32 v[50:51], v[50:51], s[30:31]
	v_pk_add_f32 v[52:53], v[52:53], s[30:31]
	v_pk_add_f32 v[54:55], v[54:55], s[30:31]
	v_rcp_f32_e32 v48, v48
	v_rcp_f32_e32 v49, v49
	v_rcp_f32_e32 v50, v50
	v_rcp_f32_e32 v51, v51
	v_rcp_f32_e32 v52, v52
	v_rcp_f32_e32 v53, v53
	v_rcp_f32_e32 v54, v54
	v_rcp_f32_e32 v55, v55
	s_nop 0
	v_pk_mul_f32 v[168:169], v[168:169], v[48:49]
	v_pk_mul_f32 v[170:171], v[170:171], v[50:51]
	v_pk_mul_f32 v[184:185], v[184:185], v[52:53]
	v_pk_mul_f32 v[186:187], v[186:187], v[54:55]
	v_cvt_pk_bf16_f32 v68, v168, v169
	v_cvt_pk_bf16_f32 v69, v170, v171
	v_cvt_pk_bf16_f32 v70, v184, v185
	v_cvt_pk_bf16_f32 v71, v186, v187
	global_store_dwordx2 v18, v[68:69], s[10:11] offset:64
	global_store_dwordx2 v18, v[70:71], s[10:11] offset:96
	v_pk_mul_f32 v[200:201], v[200:201], v[24:25] op_sel_hi:[1,0]
	v_pk_mul_f32 v[202:203], v[202:203], v[24:25] op_sel_hi:[1,0]
	v_pk_mul_f32 v[216:217], v[216:217], v[24:25] op_sel_hi:[1,0]
	v_pk_mul_f32 v[218:219], v[218:219], v[24:25] op_sel_hi:[1,0]
	v_pk_mul_f32 v[32:33], v[200:201], s[26:27]
	v_pk_mul_f32 v[34:35], v[202:203], s[26:27]
	v_pk_mul_f32 v[36:37], v[216:217], s[26:27]
	v_pk_mul_f32 v[38:39], v[218:219], s[26:27]
	v_pk_fma_f32 v[32:33], v[200:201], v[32:33], s[28:29] neg_lo:[1,0,0] neg_hi:[1,0,0]
	v_pk_fma_f32 v[34:35], v[202:203], v[34:35], s[28:29] neg_lo:[1,0,0] neg_hi:[1,0,0]
	v_pk_fma_f32 v[36:37], v[216:217], v[36:37], s[28:29] neg_lo:[1,0,0] neg_hi:[1,0,0]
	v_pk_fma_f32 v[38:39], v[218:219], v[38:39], s[28:29] neg_lo:[1,0,0] neg_hi:[1,0,0]
	v_pk_mul_f32 v[32:33], v[200:201], v[32:33]
	v_pk_mul_f32 v[34:35], v[202:203], v[34:35]
	v_pk_mul_f32 v[36:37], v[216:217], v[36:37]
	v_pk_mul_f32 v[38:39], v[218:219], v[38:39]
	v_exp_f32_e32 v32, v32
	v_exp_f32_e32 v33, v33
	v_exp_f32_e32 v34, v34
	v_exp_f32_e32 v35, v35
	v_exp_f32_e32 v36, v36
	v_exp_f32_e32 v37, v37
	v_exp_f32_e32 v38, v38
	v_exp_f32_e32 v39, v39
	v_pk_add_f32 v[32:33], v[32:33], s[30:31]
	v_pk_add_f32 v[34:35], v[34:35], s[30:31]
	v_pk_add_f32 v[36:37], v[36:37], s[30:31]
	v_pk_add_f32 v[38:39], v[38:39], s[30:31]
	v_rcp_f32_e32 v32, v32
	v_rcp_f32_e32 v33, v33
	v_rcp_f32_e32 v34, v34
	v_rcp_f32_e32 v35, v35
	v_rcp_f32_e32 v36, v36
	v_rcp_f32_e32 v37, v37
	v_rcp_f32_e32 v38, v38
	v_rcp_f32_e32 v39, v39
	s_nop 0
	v_pk_mul_f32 v[200:201], v[200:201], v[32:33]
	v_pk_mul_f32 v[202:203], v[202:203], v[34:35]
	v_pk_mul_f32 v[216:217], v[216:217], v[36:37]
	v_pk_mul_f32 v[218:219], v[218:219], v[38:39]
	v_cvt_pk_bf16_f32 v64, v200, v201
	v_cvt_pk_bf16_f32 v65, v202, v203
	v_cvt_pk_bf16_f32 v66, v216, v217
	v_cvt_pk_bf16_f32 v67, v218, v219
	global_store_dwordx2 v18, v[64:65], s[10:11] offset:128
	global_store_dwordx2 v18, v[66:67], s[10:11] offset:160
	v_pk_mul_f32 v[232:233], v[232:233], v[24:25] op_sel_hi:[1,0]
	v_pk_mul_f32 v[234:235], v[234:235], v[24:25] op_sel_hi:[1,0]
	v_pk_mul_f32 v[248:249], v[248:249], v[24:25] op_sel_hi:[1,0]
	v_pk_mul_f32 v[250:251], v[250:251], v[24:25] op_sel_hi:[1,0]
	v_pk_mul_f32 v[48:49], v[232:233], s[26:27]
	v_pk_mul_f32 v[50:51], v[234:235], s[26:27]
	v_pk_mul_f32 v[52:53], v[248:249], s[26:27]
	v_pk_mul_f32 v[54:55], v[250:251], s[26:27]
	v_pk_fma_f32 v[48:49], v[232:233], v[48:49], s[28:29] neg_lo:[1,0,0] neg_hi:[1,0,0]
	v_pk_fma_f32 v[50:51], v[234:235], v[50:51], s[28:29] neg_lo:[1,0,0] neg_hi:[1,0,0]
	v_pk_fma_f32 v[52:53], v[248:249], v[52:53], s[28:29] neg_lo:[1,0,0] neg_hi:[1,0,0]
	v_pk_fma_f32 v[54:55], v[250:251], v[54:55], s[28:29] neg_lo:[1,0,0] neg_hi:[1,0,0]
	v_pk_mul_f32 v[48:49], v[232:233], v[48:49]
	v_pk_mul_f32 v[50:51], v[234:235], v[50:51]
	v_pk_mul_f32 v[52:53], v[248:249], v[52:53]
	v_pk_mul_f32 v[54:55], v[250:251], v[54:55]
	v_exp_f32_e32 v48, v48
	v_exp_f32_e32 v49, v49
	v_exp_f32_e32 v50, v50
	v_exp_f32_e32 v51, v51
	v_exp_f32_e32 v52, v52
	v_exp_f32_e32 v53, v53
	v_exp_f32_e32 v54, v54
	v_exp_f32_e32 v55, v55
	v_pk_add_f32 v[48:49], v[48:49], s[30:31]
	v_pk_add_f32 v[50:51], v[50:51], s[30:31]
	v_pk_add_f32 v[52:53], v[52:53], s[30:31]
	v_pk_add_f32 v[54:55], v[54:55], s[30:31]
	v_rcp_f32_e32 v48, v48
	v_rcp_f32_e32 v49, v49
	v_rcp_f32_e32 v50, v50
	v_rcp_f32_e32 v51, v51
	v_rcp_f32_e32 v52, v52
	v_rcp_f32_e32 v53, v53
	v_rcp_f32_e32 v54, v54
	v_rcp_f32_e32 v55, v55
	s_nop 0
	v_pk_mul_f32 v[232:233], v[232:233], v[48:49]
	v_pk_mul_f32 v[234:235], v[234:235], v[50:51]
	v_pk_mul_f32 v[248:249], v[248:249], v[52:53]
	v_pk_mul_f32 v[250:251], v[250:251], v[54:55]
	v_cvt_pk_bf16_f32 v68, v232, v233
	v_cvt_pk_bf16_f32 v69, v234, v235
	v_cvt_pk_bf16_f32 v70, v248, v249
	v_cvt_pk_bf16_f32 v71, v250, v251
	global_store_dwordx2 v18, v[68:69], s[10:11] offset:192
	global_store_dwordx2 v18, v[70:71], s[10:11] offset:224
	v_pk_mul_f32 v[140:141], v[140:141], v[26:27] op_sel_hi:[1,0]
	v_pk_mul_f32 v[142:143], v[142:143], v[26:27] op_sel_hi:[1,0]
	v_pk_mul_f32 v[156:157], v[156:157], v[26:27] op_sel_hi:[1,0]
	v_pk_mul_f32 v[158:159], v[158:159], v[26:27] op_sel_hi:[1,0]
	v_pk_mul_f32 v[32:33], v[140:141], s[26:27]
	v_pk_mul_f32 v[34:35], v[142:143], s[26:27]
	v_pk_mul_f32 v[36:37], v[156:157], s[26:27]
	v_pk_mul_f32 v[38:39], v[158:159], s[26:27]
	v_pk_fma_f32 v[32:33], v[140:141], v[32:33], s[28:29] neg_lo:[1,0,0] neg_hi:[1,0,0]
	v_pk_fma_f32 v[34:35], v[142:143], v[34:35], s[28:29] neg_lo:[1,0,0] neg_hi:[1,0,0]
	v_pk_fma_f32 v[36:37], v[156:157], v[36:37], s[28:29] neg_lo:[1,0,0] neg_hi:[1,0,0]
	v_pk_fma_f32 v[38:39], v[158:159], v[38:39], s[28:29] neg_lo:[1,0,0] neg_hi:[1,0,0]
	v_pk_mul_f32 v[32:33], v[140:141], v[32:33]
	v_pk_mul_f32 v[34:35], v[142:143], v[34:35]
	v_pk_mul_f32 v[36:37], v[156:157], v[36:37]
	v_pk_mul_f32 v[38:39], v[158:159], v[38:39]
	v_exp_f32_e32 v32, v32
	v_exp_f32_e32 v33, v33
	v_exp_f32_e32 v34, v34
	v_exp_f32_e32 v35, v35
	v_exp_f32_e32 v36, v36
	v_exp_f32_e32 v37, v37
	v_exp_f32_e32 v38, v38
	v_exp_f32_e32 v39, v39
	v_pk_add_f32 v[32:33], v[32:33], s[30:31]
	v_pk_add_f32 v[34:35], v[34:35], s[30:31]
	v_pk_add_f32 v[36:37], v[36:37], s[30:31]
	v_pk_add_f32 v[38:39], v[38:39], s[30:31]
	v_rcp_f32_e32 v32, v32
	v_rcp_f32_e32 v33, v33
	v_rcp_f32_e32 v34, v34
	v_rcp_f32_e32 v35, v35
	v_rcp_f32_e32 v36, v36
	v_rcp_f32_e32 v37, v37
	v_rcp_f32_e32 v38, v38
	v_rcp_f32_e32 v39, v39
	s_nop 0
	v_pk_mul_f32 v[140:141], v[140:141], v[32:33]
	v_pk_mul_f32 v[142:143], v[142:143], v[34:35]
	v_pk_mul_f32 v[156:157], v[156:157], v[36:37]
	v_pk_mul_f32 v[158:159], v[158:159], v[38:39]
	v_cvt_pk_bf16_f32 v64, v140, v141
	v_cvt_pk_bf16_f32 v65, v142, v143
	v_cvt_pk_bf16_f32 v66, v156, v157
	v_cvt_pk_bf16_f32 v67, v158, v159
	global_store_dwordx2 v19, v[64:65], s[10:11]
	global_store_dwordx2 v19, v[66:67], s[10:11] offset:32
	v_pk_mul_f32 v[172:173], v[172:173], v[26:27] op_sel_hi:[1,0]
	v_pk_mul_f32 v[174:175], v[174:175], v[26:27] op_sel_hi:[1,0]
	v_pk_mul_f32 v[188:189], v[188:189], v[26:27] op_sel_hi:[1,0]
	v_pk_mul_f32 v[190:191], v[190:191], v[26:27] op_sel_hi:[1,0]
	v_pk_mul_f32 v[48:49], v[172:173], s[26:27]
	v_pk_mul_f32 v[50:51], v[174:175], s[26:27]
	v_pk_mul_f32 v[52:53], v[188:189], s[26:27]
	v_pk_mul_f32 v[54:55], v[190:191], s[26:27]
	v_pk_fma_f32 v[48:49], v[172:173], v[48:49], s[28:29] neg_lo:[1,0,0] neg_hi:[1,0,0]
	v_pk_fma_f32 v[50:51], v[174:175], v[50:51], s[28:29] neg_lo:[1,0,0] neg_hi:[1,0,0]
	v_pk_fma_f32 v[52:53], v[188:189], v[52:53], s[28:29] neg_lo:[1,0,0] neg_hi:[1,0,0]
	v_pk_fma_f32 v[54:55], v[190:191], v[54:55], s[28:29] neg_lo:[1,0,0] neg_hi:[1,0,0]
	v_pk_mul_f32 v[48:49], v[172:173], v[48:49]
	v_pk_mul_f32 v[50:51], v[174:175], v[50:51]
	v_pk_mul_f32 v[52:53], v[188:189], v[52:53]
	v_pk_mul_f32 v[54:55], v[190:191], v[54:55]
	v_exp_f32_e32 v48, v48
	v_exp_f32_e32 v49, v49
	v_exp_f32_e32 v50, v50
	v_exp_f32_e32 v51, v51
	v_exp_f32_e32 v52, v52
	v_exp_f32_e32 v53, v53
	v_exp_f32_e32 v54, v54
	v_exp_f32_e32 v55, v55
	v_pk_add_f32 v[48:49], v[48:49], s[30:31]
	v_pk_add_f32 v[50:51], v[50:51], s[30:31]
	v_pk_add_f32 v[52:53], v[52:53], s[30:31]
	v_pk_add_f32 v[54:55], v[54:55], s[30:31]
	v_rcp_f32_e32 v48, v48
	v_rcp_f32_e32 v49, v49
	v_rcp_f32_e32 v50, v50
	v_rcp_f32_e32 v51, v51
	v_rcp_f32_e32 v52, v52
	v_rcp_f32_e32 v53, v53
	v_rcp_f32_e32 v54, v54
	v_rcp_f32_e32 v55, v55
	s_nop 0
	v_pk_mul_f32 v[172:173], v[172:173], v[48:49]
	v_pk_mul_f32 v[174:175], v[174:175], v[50:51]
	v_pk_mul_f32 v[188:189], v[188:189], v[52:53]
	v_pk_mul_f32 v[190:191], v[190:191], v[54:55]
	v_cvt_pk_bf16_f32 v68, v172, v173
	v_cvt_pk_bf16_f32 v69, v174, v175
	v_cvt_pk_bf16_f32 v70, v188, v189
	v_cvt_pk_bf16_f32 v71, v190, v191
	global_store_dwordx2 v19, v[68:69], s[10:11] offset:64
	global_store_dwordx2 v19, v[70:71], s[10:11] offset:96
	v_pk_mul_f32 v[204:205], v[204:205], v[26:27] op_sel_hi:[1,0]
	v_pk_mul_f32 v[206:207], v[206:207], v[26:27] op_sel_hi:[1,0]
	v_pk_mul_f32 v[220:221], v[220:221], v[26:27] op_sel_hi:[1,0]
	v_pk_mul_f32 v[222:223], v[222:223], v[26:27] op_sel_hi:[1,0]
	v_pk_mul_f32 v[32:33], v[204:205], s[26:27]
	v_pk_mul_f32 v[34:35], v[206:207], s[26:27]
	v_pk_mul_f32 v[36:37], v[220:221], s[26:27]
	v_pk_mul_f32 v[38:39], v[222:223], s[26:27]
	v_pk_fma_f32 v[32:33], v[204:205], v[32:33], s[28:29] neg_lo:[1,0,0] neg_hi:[1,0,0]
	v_pk_fma_f32 v[34:35], v[206:207], v[34:35], s[28:29] neg_lo:[1,0,0] neg_hi:[1,0,0]
	v_pk_fma_f32 v[36:37], v[220:221], v[36:37], s[28:29] neg_lo:[1,0,0] neg_hi:[1,0,0]
	v_pk_fma_f32 v[38:39], v[222:223], v[38:39], s[28:29] neg_lo:[1,0,0] neg_hi:[1,0,0]
	v_pk_mul_f32 v[32:33], v[204:205], v[32:33]
	v_pk_mul_f32 v[34:35], v[206:207], v[34:35]
	v_pk_mul_f32 v[36:37], v[220:221], v[36:37]
	v_pk_mul_f32 v[38:39], v[222:223], v[38:39]
	v_exp_f32_e32 v32, v32
	v_exp_f32_e32 v33, v33
	v_exp_f32_e32 v34, v34
	v_exp_f32_e32 v35, v35
	v_exp_f32_e32 v36, v36
	v_exp_f32_e32 v37, v37
	v_exp_f32_e32 v38, v38
	v_exp_f32_e32 v39, v39
	v_pk_add_f32 v[32:33], v[32:33], s[30:31]
	v_pk_add_f32 v[34:35], v[34:35], s[30:31]
	v_pk_add_f32 v[36:37], v[36:37], s[30:31]
	v_pk_add_f32 v[38:39], v[38:39], s[30:31]
	v_rcp_f32_e32 v32, v32
	v_rcp_f32_e32 v33, v33
	v_rcp_f32_e32 v34, v34
	v_rcp_f32_e32 v35, v35
	v_rcp_f32_e32 v36, v36
	v_rcp_f32_e32 v37, v37
	v_rcp_f32_e32 v38, v38
	v_rcp_f32_e32 v39, v39
	s_nop 0
	v_pk_mul_f32 v[204:205], v[204:205], v[32:33]
	v_pk_mul_f32 v[206:207], v[206:207], v[34:35]
	v_pk_mul_f32 v[220:221], v[220:221], v[36:37]
	v_pk_mul_f32 v[222:223], v[222:223], v[38:39]
	v_cvt_pk_bf16_f32 v64, v204, v205
	v_cvt_pk_bf16_f32 v65, v206, v207
	v_cvt_pk_bf16_f32 v66, v220, v221
	v_cvt_pk_bf16_f32 v67, v222, v223
	global_store_dwordx2 v19, v[64:65], s[10:11] offset:128
	global_store_dwordx2 v19, v[66:67], s[10:11] offset:160
	v_pk_mul_f32 v[236:237], v[236:237], v[26:27] op_sel_hi:[1,0]
	v_pk_mul_f32 v[238:239], v[238:239], v[26:27] op_sel_hi:[1,0]
	v_pk_mul_f32 v[252:253], v[252:253], v[26:27] op_sel_hi:[1,0]
	v_pk_mul_f32 v[254:255], v[254:255], v[26:27] op_sel_hi:[1,0]
	v_pk_mul_f32 v[48:49], v[236:237], s[26:27]
	v_pk_mul_f32 v[50:51], v[238:239], s[26:27]
	v_pk_mul_f32 v[52:53], v[252:253], s[26:27]
	v_pk_mul_f32 v[54:55], v[254:255], s[26:27]
	v_pk_fma_f32 v[48:49], v[236:237], v[48:49], s[28:29] neg_lo:[1,0,0] neg_hi:[1,0,0]
	v_pk_fma_f32 v[50:51], v[238:239], v[50:51], s[28:29] neg_lo:[1,0,0] neg_hi:[1,0,0]
	v_pk_fma_f32 v[52:53], v[252:253], v[52:53], s[28:29] neg_lo:[1,0,0] neg_hi:[1,0,0]
	v_pk_fma_f32 v[54:55], v[254:255], v[54:55], s[28:29] neg_lo:[1,0,0] neg_hi:[1,0,0]
	v_pk_mul_f32 v[48:49], v[236:237], v[48:49]
	v_pk_mul_f32 v[50:51], v[238:239], v[50:51]
	v_pk_mul_f32 v[52:53], v[252:253], v[52:53]
	v_pk_mul_f32 v[54:55], v[254:255], v[54:55]
	v_exp_f32_e32 v48, v48
	v_exp_f32_e32 v49, v49
	v_exp_f32_e32 v50, v50
	v_exp_f32_e32 v51, v51
	v_exp_f32_e32 v52, v52
	v_exp_f32_e32 v53, v53
	v_exp_f32_e32 v54, v54
	v_exp_f32_e32 v55, v55
	v_pk_add_f32 v[48:49], v[48:49], s[30:31]
	v_pk_add_f32 v[50:51], v[50:51], s[30:31]
	v_pk_add_f32 v[52:53], v[52:53], s[30:31]
	v_pk_add_f32 v[54:55], v[54:55], s[30:31]
	v_rcp_f32_e32 v48, v48
	v_rcp_f32_e32 v49, v49
	v_rcp_f32_e32 v50, v50
	v_rcp_f32_e32 v51, v51
	v_rcp_f32_e32 v52, v52
	v_rcp_f32_e32 v53, v53
	v_rcp_f32_e32 v54, v54
	v_rcp_f32_e32 v55, v55
	s_nop 0
	v_pk_mul_f32 v[236:237], v[236:237], v[48:49]
	v_pk_mul_f32 v[238:239], v[238:239], v[50:51]
	v_pk_mul_f32 v[252:253], v[252:253], v[52:53]
	v_pk_mul_f32 v[254:255], v[254:255], v[54:55]
	v_cvt_pk_bf16_f32 v68, v236, v237
	v_cvt_pk_bf16_f32 v69, v238, v239
	v_cvt_pk_bf16_f32 v70, v252, v253
	v_cvt_pk_bf16_f32 v71, v254, v255
	global_store_dwordx2 v19, v[68:69], s[10:11] offset:192
	global_store_dwordx2 v19, v[70:71], s[10:11] offset:224

	.amdhsa_kernel _Z7gemm128ILi2ELi128EEv8GemmArgs
		.amdhsa_group_segment_fixed_size 81920
		.amdhsa_private_segment_fixed_size 0
		.amdhsa_kernarg_size 80
		.amdhsa_user_sgpr_count 2
		.amdhsa_user_sgpr_dispatch_ptr 0
		.amdhsa_user_sgpr_queue_ptr 0
		.amdhsa_user_sgpr_kernarg_segment_ptr 1
		.amdhsa_user_sgpr_dispatch_id 0
		.amdhsa_user_sgpr_kernarg_preload_length 0
		.amdhsa_user_sgpr_kernarg_preload_offset 0
		.amdhsa_user_sgpr_private_segment_size 0
		.amdhsa_uses_dynamic_stack 0
		.amdhsa_enable_private_segment 0
		.amdhsa_system_sgpr_workgroup_id_x 1
		.amdhsa_system_sgpr_workgroup_id_y 0
		.amdhsa_system_sgpr_workgroup_id_z 0
		.amdhsa_system_sgpr_workgroup_info 0
		.amdhsa_system_vgpr_workitem_id 0
		.amdhsa_next_free_vgpr 256
		.amdhsa_next_free_sgpr 32
		.amdhsa_accum_offset 256
		.amdhsa_reserve_vcc 1
		.amdhsa_float_round_mode_32 0
		.amdhsa_float_round_mode_16_64 0
		.amdhsa_float_denorm_mode_32 3
		.amdhsa_float_denorm_mode_16_64 3
		.amdhsa_dx10_clamp 1
		.amdhsa_ieee_mode 1
		.amdhsa_fp16_overflow 0
		.amdhsa_tg_split 0
		.amdhsa_exception_fp_ieee_invalid_op 0
		.amdhsa_exception_fp_denorm_src 0
		.amdhsa_exception_fp_ieee_div_zero 0
		.amdhsa_exception_fp_ieee_overflow 0
		.amdhsa_exception_fp_ieee_underflow 0
		.amdhsa_exception_fp_ieee_inexact 0
		.amdhsa_exception_int_div_zero 0
	.end_amdhsa_kernel

.Lfunc_end3:
	.size	_Z7gemm128ILi2ELi128EEv8GemmArgs, .Lfunc_end3-_Z7gemm128ILi2ELi128EEv8GemmArgs
	.set _Z7gemm128ILi2ELi128EEv8GemmArgs.num_vgpr, 256
	.set _Z7gemm128ILi2ELi128EEv8GemmArgs.num_agpr, 0
	.set _Z7gemm128ILi2ELi128EEv8GemmArgs.numbered_sgpr, 32
	.set _Z7gemm128ILi2ELi128EEv8GemmArgs.num_named_barrier, 0
	.set _Z7gemm128ILi2ELi128EEv8GemmArgs.private_seg_size, 0
	.set _Z7gemm128ILi2ELi128EEv8GemmArgs.uses_vcc, 1
	.set _Z7gemm128ILi2ELi128EEv8GemmArgs.uses_flat_scratch, 0
	.set _Z7gemm128ILi2ELi128EEv8GemmArgs.has_dyn_sized_stack, 0
	.set _Z7gemm128ILi2ELi128EEv8GemmArgs.has_recursion, 0
	.set _Z7gemm128ILi2ELi128EEv8GemmArgs.has_indirect_call, 0

amdhsa.kernels:
  - .agpr_count:     0
    .args:
      - .offset:         0
        .size:           136
        .value_kind:     by_value
      - .offset:         136
        .size:           4
        .value_kind:     hidden_block_count_x
      - .offset:         140
        .size:           4
        .value_kind:     hidden_block_count_y
      - .offset:         144
        .size:           4
        .value_kind:     hidden_block_count_z
      - .offset:         148
        .size:           2
        .value_kind:     hidden_group_size_x
      - .offset:         150
        .size:           2
        .value_kind:     hidden_group_size_y
      - .offset:         152
        .size:           2
        .value_kind:     hidden_group_size_z
      - .offset:         154
        .size:           2
        .value_kind:     hidden_remainder_x
      - .offset:         156
        .size:           2
        .value_kind:     hidden_remainder_y
      - .offset:         158
        .size:           2
        .value_kind:     hidden_remainder_z
      - .offset:         176
        .size:           8
        .value_kind:     hidden_global_offset_x
      - .offset:         184
        .size:           8
        .value_kind:     hidden_global_offset_y
      - .offset:         192
        .size:           8
        .value_kind:     hidden_global_offset_z
      - .offset:         200
        .size:           2
        .value_kind:     hidden_grid_dims
    .group_segment_fixed_size: 16640
    .kernarg_segment_align: 8
    .kernarg_segment_size: 392
    .language:       OpenCL C
    .language_version:
      - 2
      - 0
    .max_flat_workgroup_size: 256
    .name:           _Z11prep_kernel8PrepArgs
    .private_segment_fixed_size: 0
    .sgpr_count:     26
    .sgpr_spill_count: 0
    .symbol:         _Z11prep_kernel8PrepArgs.kd
    .uniform_work_group_size: 1
    .uses_dynamic_stack: false
    .vgpr_count:     46
    .vgpr_spill_count: 0
    .wavefront_size: 64
  - .agpr_count:     0
    .args:
      - .offset:         0
        .size:           216
        .value_kind:     by_value
    .group_segment_fixed_size: 0
    .kernarg_segment_align: 8
    .kernarg_segment_size: 216
    .language:       OpenCL C
    .language_version:
      - 2
      - 0
    .max_flat_workgroup_size: 512
    .name:           _Z11attn_kernel8AttnArgs
    .private_segment_fixed_size: 0
    .sgpr_count:     82
    .sgpr_spill_count: 0
    .symbol:         _Z11attn_kernel8AttnArgs.kd
    .uniform_work_group_size: 1
    .uses_dynamic_stack: false
    .vgpr_count:     220
    .vgpr_spill_count: 0
    .wavefront_size: 64
  - .agpr_count:     0
    .args:
      - .offset:         0
        .size:           80
        .value_kind:     by_value
    .group_segment_fixed_size: 98304
    .kernarg_segment_align: 8
    .kernarg_segment_size: 80
    .language:       OpenCL C
    .language_version:
      - 2
      - 0
    .max_flat_workgroup_size: 256
    .name:           _Z7gemm128ILi1ELi96EEv8GemmArgs
    .private_segment_fixed_size: 0
    .sgpr_count:     37
    .sgpr_spill_count: 0
    .symbol:         _Z7gemm128ILi1ELi96EEv8GemmArgs.kd
    .uniform_work_group_size: 1
    .uses_dynamic_stack: false
    .vgpr_count:     256
    .vgpr_spill_count: 0
    .wavefront_size: 64
  - .agpr_count:     0
    .args:
      - .offset:         0
        .size:           80
        .value_kind:     by_value
    .group_segment_fixed_size: 81920
    .kernarg_segment_align: 8
    .kernarg_segment_size: 80
    .language:       OpenCL C
    .language_version:
      - 2
      - 0
    .max_flat_workgroup_size: 256
    .name:           _Z7gemm128ILi2ELi128EEv8GemmArgs
    .private_segment_fixed_size: 0
    .sgpr_count:     38
    .sgpr_spill_count: 0
    .symbol:         _Z7gemm128ILi2ELi128EEv8GemmArgs.kd
    .uniform_work_group_size: 1
    .uses_dynamic_stack: false
    .vgpr_count:     256
    .vgpr_spill_count: 0
    .wavefront_size: 64
  - .agpr_count:     0
    .args:
      - .offset:         0
        .size:           80
        .value_kind:     by_value
    .group_segment_fixed_size: 98304
    .kernarg_segment_align: 8
    .kernarg_segment_size: 80
    .language:       OpenCL C
    .language_version:
      - 2
      - 0
    .max_flat_workgroup_size: 256
    .name:           _Z7gemm128ILi3ELi96EEv8GemmArgs
    .private_segment_fixed_size: 0
    .sgpr_count:     30
    .sgpr_spill_count: 0
    .symbol:         _Z7gemm128ILi3ELi96EEv8GemmArgs.kd
    .uniform_work_group_size: 1
    .uses_dynamic_stack: false
    .vgpr_count:     256
    .vgpr_spill_count: 0
    .wavefront_size: 64
  - .agpr_count:     0
    .args:
      - .offset:         0
        .size:           32
        .value_kind:     by_value
      - .offset:         32
        .size:           56
        .value_kind:     by_value
    .group_segment_fixed_size: 0
    .kernarg_segment_align: 8
    .kernarg_segment_size: 88
    .language:       OpenCL C
    .language_version:
      - 2
      - 0
    .max_flat_workgroup_size: 512
    .name:           _Z8gemm_bigIN3pg86EpiQKVEEvNS0_4GemmET_
    .private_segment_fixed_size: 0
    .sgpr_count:     58
    .sgpr_spill_count: 0
    .symbol:         _Z8gemm_bigIN3pg86EpiQKVEEvNS0_4GemmET_.kd
    .uniform_work_group_size: 1
    .uses_dynamic_stack: false
    .vgpr_count:     228
    .vgpr_spill_count: 0
    .wavefront_size: 64
  - .agpr_count:     0
    .args:
      - .offset:         0
        .size:           32
        .value_kind:     by_value
      - .offset:         32
        .size:           32
        .value_kind:     by_value
    .group_segment_fixed_size: 0
    .kernarg_segment_align: 8
    .kernarg_segment_size: 64
    .language:       OpenCL C
    .language_version:
      - 2
      - 0
    .max_flat_workgroup_size: 512
    .name:           _Z8gemm_bigIN3pg85EpiUPEEvNS0_4GemmET_
    .private_segment_fixed_size: 0
    .sgpr_count:     50
    .sgpr_spill_count: 0
    .symbol:         _Z8gemm_bigIN3pg85EpiUPEEvNS0_4GemmET_.kd
    .uniform_work_group_size: 1
    .uses_dynamic_stack: false
    .vgpr_count:     226
    .vgpr_spill_count: 0
    .wavefront_size: 64
